# v50 with the nt hint removed from every plain global load (streaming phases included)
# baseline (speedup 1.0000x reference)
; __device__ __forceinline__ void p0_mod(const Args& a, LAS unsigned char* lds) {
;     ...
;         for (int d0 = dch * 64; d0 < dch * 64 + 64; d0 += 16) {
;             float wv[16];
; #pragma unroll
;             for (int k = 0; k < 16; ++k) wv[k] = __builtin_nontemporal_load(w + (size_t)(d0 + k) * 6144);
; #pragma unroll
;             for (int k = 0; k < 16; ++k)
; #pragma unroll
;                 for (int b = 0; b < 8; ++b) acc[b] += cs[b * D + d0 + k] * wv[k];
;         }
.LBB0_11:
	v_add_co_u32_e32 v144, vcc, 0xfffa6000, v142
	ds_read_b128 v[18:21], v148
	ds_read_b128 v[14:17], v148 offset:16
	ds_read_b128 v[10:13], v148 offset:4096
	ds_read_b128 v[22:25], v148 offset:4112
	ds_read_b128 v[66:69], v148 offset:32
	ds_read_b128 v[54:57], v148 offset:48
	ds_read_b128 v[26:29], v148 offset:4128
	ds_read_b128 v[30:33], v148 offset:4144
	ds_read_b128 v[82:85], v148 offset:8192
	ds_read_b128 v[78:81], v148 offset:8208
	ds_read_b128 v[38:41], v148 offset:12288
	ds_read_b128 v[34:37], v148 offset:12304
	ds_read_b128 v[90:93], v148 offset:8224
	ds_read_b128 v[98:101], v148 offset:8240
	ds_read_b128 v[46:49], v148 offset:12320
	ds_read_b128 v[42:45], v148 offset:12336
	ds_read_b128 v[118:121], v148 offset:16384
	ds_read_b128 v[106:109], v148 offset:16400
	ds_read_b128 v[58:61], v148 offset:20480
	ds_read_b128 v[50:53], v148 offset:20496
	ds_read_b128 v[130:133], v148 offset:24576
	ds_read_b128 v[110:113], v148 offset:24592
	ds_read_b128 v[70:73], v148 offset:28672
	ds_read_b128 v[62:65], v148 offset:28688
	ds_read_b128 v[150:153], v148 offset:16416
	ds_read_b128 v[114:117], v148 offset:16432
	ds_read_b128 v[86:89], v148 offset:20512
	ds_read_b128 v[74:77], v148 offset:20528
	ds_read_b128 v[122:125], v148 offset:24608
	ds_read_b128 v[126:129], v148 offset:24624
	ds_read_b128 v[102:105], v148 offset:28704
	ds_read_b128 v[94:97], v148 offset:28720
	v_addc_co_u32_e32 v145, vcc, -1, v143, vcc
	v_add_co_u32_e32 v154, vcc, 0xfffac000, v142
	s_waitcnt lgkmcnt(0)
	v_mov_b32_e32 v170, v130
	v_addc_co_u32_e32 v155, vcc, -1, v143, vcc
	v_add_co_u32_e32 v156, vcc, 0xfffb2000, v142
	v_mov_b32_e32 v130, v114
	s_nop 0
	v_addc_co_u32_e32 v157, vcc, -1, v143, vcc
	v_add_co_u32_e32 v158, vcc, 0xfffb8000, v142
	v_mov_b32_e32 v171, v70
	s_nop 0
	v_addc_co_u32_e32 v159, vcc, -1, v143, vcc
	v_add_co_u32_e32 v160, vcc, 0xfffbe000, v142
	v_mov_b32_e32 v70, v131
	s_nop 0
	v_addc_co_u32_e32 v161, vcc, -1, v143, vcc
	v_add_co_u32_e32 v162, vcc, 0xfffc4000, v142
	v_mov_b32_e32 v131, v74
	s_nop 0
	v_addc_co_u32_e32 v163, vcc, -1, v143, vcc
	v_add_co_u32_e32 v114, vcc, 0xfffca000, v142
	v_mov_b32_e32 v74, v115
	s_nop 0
	v_addc_co_u32_e32 v115, vcc, -1, v143, vcc
	v_mov_b32_e32 v166, v82
	v_mov_b32_e32 v82, v120
	v_mov_b32_e32 v120, v152
	v_add_co_u32_e32 v152, vcc, 0xfffd0000, v142
	v_mov_b32_e32 v167, v38
	v_mov_b32_e32 v38, v83
	v_mov_b32_e32 v83, v60
	v_mov_b32_e32 v60, v121
	v_mov_b32_e32 v121, v88
	v_mov_b32_e32 v88, v153
	v_addc_co_u32_e32 v153, vcc, -1, v143, vcc
	global_load_dword v144, v[144:145], off
	s_nop 0
	global_load_dword v154, v[154:155], off
	s_nop 0
	global_load_dword v156, v[156:157], off
	s_nop 0
	global_load_dword v158, v[158:159], off
	v_mov_b32_e32 v164, v18
	v_mov_b32_e32 v168, v118
	v_mov_b32_e32 v18, v20
	v_mov_b32_e32 v20, v84
	v_mov_b32_e32 v84, v132
	v_mov_b32_e32 v118, v14
	v_mov_b32_e32 v14, v16
	v_mov_b32_e32 v16, v66
	v_mov_b32_e32 v66, v68
	v_mov_b32_e32 v68, v54
	v_mov_b32_e32 v54, v56
	v_mov_b32_e32 v56, v78
	v_mov_b32_e32 v78, v80
	v_mov_b32_e32 v80, v90
	v_mov_b32_e32 v90, v92
	v_mov_b32_e32 v92, v98
	v_mov_b32_e32 v98, v100
	v_mov_b32_e32 v100, v106
	v_mov_b32_e32 v106, v108
	v_mov_b32_e32 v108, v110
	v_mov_b32_e32 v110, v112
	v_mov_b32_e32 v112, v150
	global_load_dword v132, v[160:161], off
	global_load_dword v150, v[162:163], off
	v_add_co_u32_e32 v160, vcc, 0xfffd6000, v142
	global_load_dword v114, v[114:115], off
	s_nop 0
	global_load_dword v152, v[152:153], off
	v_addc_co_u32_e32 v161, vcc, -1, v143, vcc
	v_add_co_u32_e32 v162, vcc, 0xfffdc000, v142
	global_load_dword v160, v[160:161], off
	s_nop 0
	v_addc_co_u32_e32 v163, vcc, -1, v143, vcc
	v_add_co_u32_e32 v172, vcc, 0xfffe2000, v142
	global_load_dword v162, v[162:163], off
	s_nop 0
	v_addc_co_u32_e32 v173, vcc, -1, v143, vcc
	v_add_co_u32_e32 v174, vcc, 0xfffe8000, v142
	v_mov_b32_e32 v165, v10
	s_nop 0
	v_addc_co_u32_e32 v175, vcc, -1, v143, vcc
	v_add_co_u32_e32 v176, vcc, 0xfffee000, v142
	global_load_dword v172, v[172:173], off
	s_nop 0
	global_load_dword v174, v[174:175], off
	v_addc_co_u32_e32 v177, vcc, -1, v143, vcc
	v_add_co_u32_e32 v178, vcc, 0xffff4000, v142
	global_load_dword v176, v[176:177], off
	s_nop 0
	v_addc_co_u32_e32 v179, vcc, -1, v143, vcc
	v_add_co_u32_e32 v180, vcc, 0xffffa000, v142
	global_load_dword v178, v[178:179], off
	s_nop 0
	v_addc_co_u32_e32 v181, vcc, -1, v143, vcc
	global_load_dword v180, v[180:181], off
	s_nop 0
	global_load_dword v182, v[142:143], off
	v_mov_b32_e32 v169, v58
	v_mov_b32_e32 v10, v19
	v_mov_b32_e32 v58, v119
	v_mov_b32_e32 v19, v12
	v_mov_b32_e32 v12, v21
	v_mov_b32_e32 v21, v40
	v_mov_b32_e32 v40, v85
	v_mov_b32_e32 v85, v72
	v_mov_b32_e32 v72, v133
	v_mov_b32_e32 v119, v22
	v_mov_b32_e32 v22, v15
	v_mov_b32_e32 v15, v24
	v_mov_b32_e32 v24, v17
	v_mov_b32_e32 v17, v26
	v_mov_b32_e32 v26, v67
	v_mov_b32_e32 v67, v28
	v_mov_b32_e32 v28, v69
	v_mov_b32_e32 v69, v30
	s_waitcnt vmcnt(15)
	v_pk_fma_f32 v[6:7], v[144:145], v[164:165], v[6:7] op_sel_hi:[0,1,1]
	v_pk_fma_f32 v[8:9], v[144:145], v[166:167], v[8:9] op_sel_hi:[0,1,1]
	v_pk_fma_f32 v[2:3], v[144:145], v[168:169], v[2:3] op_sel_hi:[0,1,1]
	v_pk_fma_f32 v[4:5], v[144:145], v[170:171], v[4:5] op_sel_hi:[0,1,1]
	s_waitcnt vmcnt(14)
	v_pk_fma_f32 v[6:7], v[154:155], v[10:11], v[6:7] op_sel_hi:[0,1,1]
	v_pk_fma_f32 v[8:9], v[154:155], v[38:39], v[8:9] op_sel_hi:[0,1,1]
	v_pk_fma_f32 v[2:3], v[154:155], v[58:59], v[2:3] op_sel_hi:[0,1,1]
	v_pk_fma_f32 v[4:5], v[154:155], v[70:71], v[4:5] op_sel_hi:[0,1,1]
	s_waitcnt vmcnt(13)
; __device__ __forceinline__ void p0_mod(const Args& a, LAS unsigned char* lds) {
;     ...
;         for (int d0 = dch * 64; d0 < dch * 64 + 64; d0 += 16) {
;             float wv[16];
; #pragma unroll
;             for (int k = 0; k < 16; ++k) wv[k] = __builtin_nontemporal_load(w + (size_t)(d0 + k) * 6144);
; #pragma unroll
;             for (int k = 0; k < 16; ++k)
; #pragma unroll
;                 for (int b = 0; b < 8; ++b) acc[b] += cs[b * D + d0 + k] * wv[k];
;         }
	v_pk_fma_f32 v[6:7], v[156:157], v[18:19], v[6:7] op_sel_hi:[0,1,1]
	v_pk_fma_f32 v[8:9], v[156:157], v[20:21], v[8:9] op_sel_hi:[0,1,1]
	v_pk_fma_f32 v[2:3], v[156:157], v[82:83], v[2:3] op_sel_hi:[0,1,1]
	v_pk_fma_f32 v[4:5], v[156:157], v[84:85], v[4:5] op_sel_hi:[0,1,1]
	v_mov_b32_e32 v30, v55
	v_mov_b32_e32 v55, v32
	v_mov_b32_e32 v32, v57
	v_mov_b32_e32 v57, v34
	v_mov_b32_e32 v34, v79
	v_mov_b32_e32 v79, v36
	v_mov_b32_e32 v36, v81
	v_mov_b32_e32 v81, v46
	v_mov_b32_e32 v46, v91
	v_mov_b32_e32 v91, v48
	v_mov_b32_e32 v48, v93
	v_mov_b32_e32 v93, v42
	v_mov_b32_e32 v42, v99
	v_mov_b32_e32 v99, v44
	v_mov_b32_e32 v44, v101
	v_mov_b32_e32 v101, v50
	v_mov_b32_e32 v50, v107
	v_mov_b32_e32 v107, v52
	v_mov_b32_e32 v52, v109
	v_mov_b32_e32 v109, v62
	s_waitcnt vmcnt(12)
	v_pk_fma_f32 v[6:7], v[158:159], v[12:13], v[6:7] op_sel_hi:[0,1,1]
	v_pk_fma_f32 v[8:9], v[158:159], v[40:41], v[8:9] op_sel_hi:[0,1,1]
	v_pk_fma_f32 v[2:3], v[158:159], v[60:61], v[2:3] op_sel_hi:[0,1,1]
	v_pk_fma_f32 v[4:5], v[158:159], v[72:73], v[4:5] op_sel_hi:[0,1,1]
	v_mov_b32_e32 v62, v111
	s_waitcnt vmcnt(11)
	v_pk_fma_f32 v[6:7], v[132:133], v[118:119], v[6:7] op_sel_hi:[0,1,1]
	v_pk_fma_f32 v[8:9], v[132:133], v[56:57], v[8:9] op_sel_hi:[0,1,1]
	v_pk_fma_f32 v[2:3], v[132:133], v[100:101], v[2:3] op_sel_hi:[0,1,1]
	v_pk_fma_f32 v[4:5], v[132:133], v[108:109], v[4:5] op_sel_hi:[0,1,1]
	v_mov_b32_e32 v111, v64
	s_waitcnt vmcnt(10)
	v_pk_fma_f32 v[6:7], v[150:151], v[22:23], v[6:7] op_sel_hi:[0,1,1]
	v_pk_fma_f32 v[8:9], v[150:151], v[34:35], v[8:9] op_sel_hi:[0,1,1]
	v_pk_fma_f32 v[2:3], v[150:151], v[50:51], v[2:3] op_sel_hi:[0,1,1]
	v_pk_fma_f32 v[4:5], v[150:151], v[62:63], v[4:5] op_sel_hi:[0,1,1]
	v_mov_b32_e32 v64, v113
	s_waitcnt vmcnt(9)
	v_pk_fma_f32 v[6:7], v[114:115], v[14:15], v[6:7] op_sel_hi:[0,1,1]
	v_pk_fma_f32 v[8:9], v[114:115], v[78:79], v[8:9] op_sel_hi:[0,1,1]
	v_pk_fma_f32 v[2:3], v[114:115], v[106:107], v[2:3] op_sel_hi:[0,1,1]
	v_pk_fma_f32 v[4:5], v[114:115], v[110:111], v[4:5] op_sel_hi:[0,1,1]
	v_mov_b32_e32 v113, v86
	v_mov_b32_e32 v184, v116
	v_mov_b32_e32 v185, v76
	v_mov_b32_e32 v76, v117
	v_mov_b32_e32 v116, v122
	v_mov_b32_e32 v117, v102
	s_waitcnt vmcnt(8)
	v_pk_fma_f32 v[6:7], v[152:153], v[24:25], v[6:7] op_sel_hi:[0,1,1]
	v_pk_fma_f32 v[8:9], v[152:153], v[36:37], v[8:9] op_sel_hi:[0,1,1]
	v_pk_fma_f32 v[2:3], v[152:153], v[52:53], v[2:3] op_sel_hi:[0,1,1]
	v_pk_fma_f32 v[4:5], v[152:153], v[64:65], v[4:5] op_sel_hi:[0,1,1]
	v_mov_b32_e32 v86, v151
	v_mov_b32_e32 v102, v123
	s_waitcnt vmcnt(7)
	v_pk_fma_f32 v[6:7], v[160:161], v[16:17], v[6:7] op_sel_hi:[0,1,1]
	v_pk_fma_f32 v[8:9], v[160:161], v[80:81], v[8:9] op_sel_hi:[0,1,1]
	v_pk_fma_f32 v[2:3], v[160:161], v[112:113], v[2:3] op_sel_hi:[0,1,1]
	v_pk_fma_f32 v[4:5], v[160:161], v[116:117], v[4:5] op_sel_hi:[0,1,1]
	v_mov_b32_e32 v122, v124
	v_mov_b32_e32 v123, v104
	s_waitcnt vmcnt(6)
	v_pk_fma_f32 v[6:7], v[162:163], v[26:27], v[6:7] op_sel_hi:[0,1,1]
	v_pk_fma_f32 v[8:9], v[162:163], v[46:47], v[8:9] op_sel_hi:[0,1,1]
	v_pk_fma_f32 v[2:3], v[162:163], v[86:87], v[2:3] op_sel_hi:[0,1,1]
	v_pk_fma_f32 v[4:5], v[162:163], v[102:103], v[4:5] op_sel_hi:[0,1,1]
	v_mov_b32_e32 v104, v125
	s_waitcnt vmcnt(5)
	v_pk_fma_f32 v[6:7], v[172:173], v[66:67], v[6:7] op_sel_hi:[0,1,1]
	v_pk_fma_f32 v[8:9], v[172:173], v[90:91], v[8:9] op_sel_hi:[0,1,1]
	v_pk_fma_f32 v[2:3], v[172:173], v[120:121], v[2:3] op_sel_hi:[0,1,1]
	v_pk_fma_f32 v[4:5], v[172:173], v[122:123], v[4:5] op_sel_hi:[0,1,1]
	v_mov_b32_e32 v124, v126
	v_mov_b32_e32 v125, v94
	s_waitcnt vmcnt(4)
	v_pk_fma_f32 v[6:7], v[174:175], v[28:29], v[6:7] op_sel_hi:[0,1,1]
	v_pk_fma_f32 v[8:9], v[174:175], v[48:49], v[8:9] op_sel_hi:[0,1,1]
	v_pk_fma_f32 v[2:3], v[174:175], v[88:89], v[2:3] op_sel_hi:[0,1,1]
	v_pk_fma_f32 v[4:5], v[174:175], v[104:105], v[4:5] op_sel_hi:[0,1,1]
	v_mov_b32_e32 v94, v127
	s_waitcnt vmcnt(3)
	v_pk_fma_f32 v[6:7], v[176:177], v[68:69], v[6:7] op_sel_hi:[0,1,1]
	v_pk_fma_f32 v[8:9], v[176:177], v[92:93], v[8:9] op_sel_hi:[0,1,1]
	v_pk_fma_f32 v[2:3], v[176:177], v[130:131], v[2:3] op_sel_hi:[0,1,1]
	v_pk_fma_f32 v[4:5], v[176:177], v[124:125], v[4:5] op_sel_hi:[0,1,1]
	v_add_u32_e32 v149, 16, v149
	v_mov_b32_e32 v126, v128
	v_mov_b32_e32 v127, v96
	s_waitcnt vmcnt(2)
	v_pk_fma_f32 v[6:7], v[178:179], v[30:31], v[6:7] op_sel_hi:[0,1,1]
	v_pk_fma_f32 v[8:9], v[178:179], v[42:43], v[8:9] op_sel_hi:[0,1,1]
	v_pk_fma_f32 v[2:3], v[178:179], v[74:75], v[2:3] op_sel_hi:[0,1,1]
	v_pk_fma_f32 v[4:5], v[178:179], v[94:95], v[4:5] op_sel_hi:[0,1,1]
	v_cmp_ge_i32_e64 s[6:7], v149, v1
	v_mov_b32_e32 v96, v129
	s_waitcnt vmcnt(1)
	v_pk_fma_f32 v[6:7], v[180:181], v[54:55], v[6:7] op_sel_hi:[0,1,1]
	v_pk_fma_f32 v[8:9], v[180:181], v[98:99], v[8:9] op_sel_hi:[0,1,1]
	v_pk_fma_f32 v[2:3], v[180:181], v[184:185], v[2:3] op_sel_hi:[0,1,1]
	v_pk_fma_f32 v[4:5], v[180:181], v[126:127], v[4:5] op_sel_hi:[0,1,1]
	v_add_u32_e32 v148, 64, v148
	s_or_b64 s[14:15], s[6:7], s[14:15]
	v_lshl_add_u64 v[142:143], v[142:143], 0, s[8:9]
	s_waitcnt vmcnt(0)
	v_pk_fma_f32 v[6:7], v[182:183], v[32:33], v[6:7] op_sel_hi:[0,1,1]
	v_pk_fma_f32 v[8:9], v[182:183], v[44:45], v[8:9] op_sel_hi:[0,1,1]
	v_pk_fma_f32 v[2:3], v[182:183], v[76:77], v[2:3] op_sel_hi:[0,1,1]
	v_pk_fma_f32 v[4:5], v[182:183], v[96:97], v[4:5] op_sel_hi:[0,1,1]
	s_andn2_b64 exec, exec, s[14:15]
	s_cbranch_execnz .LBB0_11
; __device__ __forceinline__ void p0_mod(const Args& a, LAS unsigned char* lds) {
;     ...
; #pragma unroll
;         for (int b = 0; b < 8; ++b) red[(dch * 32 + el) * 8 + b] = acc[b];
;         __syncthreads();
;         if (tid < 256) {
;             const int e2 = tid & 31, b = tid >> 5; float s = 0.f;
;             for (int k = 0; k < 16; ++k) s += red[(k * 32 + e2) * 8 + b];
;             mod[((size_t)l * NB + b) * 6144 + e0 + e2] = s + a.in[I_ADAB][l * 6144 + e0 + e2];
;         }
;         __syncthreads();
	s_or_b64 exec, exec, s[14:15]
	ds_write_b128 v146, v[6:9] offset:32768
	ds_write_b128 v146, v[2:5] offset:32784
	s_waitcnt lgkmcnt(0)
	s_barrier
	s_and_saveexec_b64 s[6:7], s[4:5]
	s_cbranch_execz .LBB0_9
	s_mul_i32 s14, s17, 0x1800
	s_add_i32 s14, s14, s12
	v_or_b32_e32 v2, s14, v134
	v_ashrrev_i32_e32 v3, 31, v2
	v_lshl_add_u64 v[2:3], v[2:3], 2, s[10:11]
	global_load_dword v20, v[2:3], off
	ds_read2st64_b32 v[2:3], v147 offset0:128 offset1:132
	ds_read2st64_b32 v[4:5], v147 offset0:136 offset1:140
	ds_read2st64_b32 v[6:7], v147 offset0:144 offset1:148
	ds_read2st64_b32 v[8:9], v147 offset0:152 offset1:156
	ds_read2st64_b32 v[10:11], v147 offset0:160 offset1:164
	ds_read2st64_b32 v[12:13], v147 offset0:168 offset1:172
	ds_read2st64_b32 v[14:15], v147 offset0:176 offset1:180
	ds_read2st64_b32 v[16:17], v147 offset0:184 offset1:188
	s_waitcnt lgkmcnt(7)
	v_add_f32_e32 v2, 0, v2
	v_add_f32_e32 v2, v2, v3
	s_waitcnt lgkmcnt(6)
	v_add_f32_e32 v2, v2, v4
	v_add_f32_e32 v2, v2, v5
	s_waitcnt lgkmcnt(5)
	v_add_f32_e32 v2, v2, v6
	v_add_f32_e32 v2, v2, v7
	s_waitcnt lgkmcnt(4)
	v_add_f32_e32 v2, v2, v8
	v_add_f32_e32 v2, v2, v9
	s_waitcnt lgkmcnt(3)
	v_add_f32_e32 v2, v2, v10
	v_add_f32_e32 v2, v2, v11
	s_waitcnt lgkmcnt(2)
	v_add_f32_e32 v2, v2, v12
	v_add_f32_e32 v2, v2, v13
	s_waitcnt lgkmcnt(1)
	v_add_f32_e32 v2, v2, v14
	v_lshl_add_u32 v21, s17, 3, v136
	v_mov_b64_e32 v[18:19], s[0:1]
	v_add_f32_e32 v2, v2, v15
	v_mad_i64_i32 v[18:19], s[14:15], v21, s3, v[18:19]
	s_waitcnt lgkmcnt(0)
	v_add_f32_e32 v2, v2, v16
	v_lshl_add_u64 v[18:19], s[12:13], 2, v[18:19]
	v_add_f32_e32 v2, v2, v17
	s_waitcnt vmcnt(0)
	v_add_f32_e32 v4, v2, v20
	v_lshl_add_u64 v[2:3], v[18:19], 0, v[138:139]
	global_store_dword v[2:3], v4, off
	s_branch .LBB0_9

; #define LAS __attribute__((address_space(3)))
;     ...
;     LAS float* scr = (LAS float*)(lds + 49152) + wave * (64 * 33);
;     const int gw = ((int)blockIdx.x - blk0) * NWAVES + wave, ngw = nblk * NWAVES;
;     constexpr int I_L = 16 * 104 + 16 * 32 + 16 * 16 * 32 + 16 * 8 * 32;
;     if ((int)blockIdx.x < blk0 || (int)blockIdx.x >= blk0 + nblk) return;
;     float tv[32];
;     const int I_E = it_hi < I_L ? it_hi : I_L;
;     int it = it_lo + gw;
;     if (it < I_E) { const PrepItem p = prep_decode(a, l, it);
; #pragma unroll
;         for (int i = 0; i < 32; ++i) tv[i] = __builtin_nontemporal_load(p.src + (size_t)(2 * i + (lane >> 5)) * p.ldw + (lane & 31)); }
.LBB0_28:
	s_or_b64 exec, exec, s[4:5]
	v_bfe_u32 v33, v1, 5, 1
	v_or_b32_e32 v49, 10, v33
	v_mul_u32_u24_e32 v15, v14, v49
	v_or_b32_e32 v50, 12, v33
	v_lshlrev_b32_e32 v16, 2, v15
	v_mul_u32_u24_e32 v15, v14, v50
	v_or_b32_e32 v51, 14, v33
	v_lshlrev_b32_e32 v18, 2, v15
	v_mul_u32_u24_e32 v15, v14, v51
	v_or_b32_e32 v52, 16, v33
	v_lshlrev_b32_e32 v20, 2, v15
	v_mul_u32_u24_e32 v15, v14, v52
	v_or_b32_e32 v53, 18, v33
	v_lshlrev_b32_e32 v22, 2, v15
	v_mul_u32_u24_e32 v15, v14, v53
	v_or_b32_e32 v54, 20, v33
	v_lshlrev_b32_e32 v24, 2, v15
	v_mul_u32_u24_e32 v15, v14, v54
	v_or_b32_e32 v55, 22, v33
	v_lshlrev_b32_e32 v26, 2, v15
	v_mul_u32_u24_e32 v15, v14, v55
	v_or_b32_e32 v56, 24, v33
	s_movk_i32 s2, 0x2100
	v_lshlrev_b32_e32 v28, 2, v15
	v_mul_u32_u24_e32 v15, v14, v56
	v_or_b32_e32 v57, 26, v33
	v_mul_lo_u32 v2, v2, s2
	v_lshlrev_b32_e32 v30, 2, v15
	v_mul_u32_u24_e32 v15, v14, v57
	v_or_b32_e32 v58, 28, v33
	v_add_u32_e32 v3, 0, v2
	v_and_b32_e32 v2, 31, v1
	v_lshlrev_b32_e32 v42, 2, v15
	v_mul_u32_u24_e32 v15, v14, v58
	v_or_b32_e32 v59, 30, v33
	v_mov_b32_e32 v35, 0
	v_lshlrev_b32_e32 v34, 2, v2
	v_lshlrev_b32_e32 v44, 2, v15
	v_mul_u32_u24_e32 v15, v14, v59
	v_lshl_add_u64 v[40:41], v[4:5], 0, v[34:35]
	v_lshlrev_b32_e32 v60, 2, v15
	v_mov_b32_e32 v61, v35
	v_lshl_add_u64 v[92:93], v[40:41], 0, v[60:61]
	v_or_b32_e32 v60, 32, v33
	v_mul_u32_u24_e32 v15, v14, v60
	v_or_b32_e32 v61, 34, v33
	v_lshlrev_b32_e32 v62, 2, v15
	v_mov_b32_e32 v63, v35
	v_mul_u32_u24_e32 v15, v14, v61
	v_lshl_add_u64 v[94:95], v[40:41], 0, v[62:63]
	v_lshlrev_b32_e32 v62, 2, v15
	v_lshl_add_u64 v[96:97], v[40:41], 0, v[62:63]
	v_or_b32_e32 v62, 36, v33
	v_mul_u32_u24_e32 v15, v14, v62
	v_or_b32_e32 v63, 38, v33
	v_lshlrev_b32_e32 v64, 2, v15
	v_mov_b32_e32 v65, v35
	v_mul_u32_u24_e32 v15, v14, v63
	v_lshl_add_u64 v[98:99], v[40:41], 0, v[64:65]
	v_lshlrev_b32_e32 v64, 2, v15
	v_lshl_add_u64 v[100:101], v[40:41], 0, v[64:65]
	v_or_b32_e32 v64, 40, v33
	v_mul_u32_u24_e32 v15, v14, v64
	v_or_b32_e32 v65, 42, v33
	v_lshlrev_b32_e32 v66, 2, v15
	v_mov_b32_e32 v67, v35
	v_mul_u32_u24_e32 v15, v14, v65
	v_lshl_add_u64 v[102:103], v[40:41], 0, v[66:67]
	v_lshlrev_b32_e32 v66, 2, v15
	v_lshl_add_u64 v[104:105], v[40:41], 0, v[66:67]
	v_or_b32_e32 v66, 44, v33
	v_mul_u32_u24_e32 v15, v14, v66
	v_or_b32_e32 v67, 46, v33
	v_lshlrev_b32_e32 v68, 2, v15
	v_mov_b32_e32 v69, v35
	v_mul_u32_u24_e32 v15, v14, v67
	v_lshl_add_u64 v[106:107], v[40:41], 0, v[68:69]
	v_lshlrev_b32_e32 v68, 2, v15
	v_lshl_add_u64 v[108:109], v[40:41], 0, v[68:69]
	v_or_b32_e32 v68, 48, v33
	v_mul_u32_u24_e32 v15, v14, v68
	v_or_b32_e32 v69, 50, v33
	v_lshlrev_b32_e32 v70, 2, v15
	v_mov_b32_e32 v71, v35
	v_mul_u32_u24_e32 v15, v14, v69
	v_lshl_add_u64 v[110:111], v[40:41], 0, v[70:71]
	v_lshlrev_b32_e32 v70, 2, v15
	v_lshl_add_u64 v[112:113], v[40:41], 0, v[70:71]
	v_or_b32_e32 v70, 52, v33
	v_mul_u32_u24_e32 v15, v14, v70
	v_or_b32_e32 v71, 54, v33
	v_lshlrev_b32_e32 v72, 2, v15
	v_mov_b32_e32 v73, v35
	v_mul_u32_u24_e32 v15, v14, v71
	v_lshl_add_u64 v[114:115], v[40:41], 0, v[72:73]
	v_lshlrev_b32_e32 v72, 2, v15
	v_lshl_add_u64 v[116:117], v[40:41], 0, v[72:73]
	v_or_b32_e32 v72, 56, v33
	v_mul_u32_u24_e32 v15, v14, v72
	v_or_b32_e32 v73, 58, v33
	v_lshlrev_b32_e32 v74, 2, v15
	v_mov_b32_e32 v75, v35
	v_mul_u32_u24_e32 v15, v14, v73
	v_lshl_add_u64 v[118:119], v[40:41], 0, v[74:75]
	v_lshlrev_b32_e32 v74, 2, v15
	v_lshl_add_u64 v[120:121], v[40:41], 0, v[74:75]
	v_or_b32_e32 v74, 60, v33
	v_or_b32_e32 v37, 2, v33
	v_or_b32_e32 v46, 4, v33
	v_or_b32_e32 v47, 6, v33
	v_or_b32_e32 v48, 8, v33
	v_mul_u32_u24_e32 v15, v14, v74
	v_or_b32_e32 v75, 62, v33
	v_mul_u32_u24_e32 v4, v14, v33
	v_mul_u32_u24_e32 v6, v14, v37
	v_mul_u32_u24_e32 v8, v14, v46
	v_mul_u32_u24_e32 v10, v14, v47
	v_mul_u32_u24_e32 v12, v14, v48
	v_lshlrev_b32_e32 v76, 2, v15
	v_mov_b32_e32 v77, v35
	v_mul_u32_u24_e32 v14, v14, v75
	v_lshlrev_b32_e32 v4, 2, v4
	v_mov_b32_e32 v5, v35
	v_lshlrev_b32_e32 v6, 2, v6
	v_mov_b32_e32 v7, v35
	v_lshlrev_b32_e32 v8, 2, v8
	v_mov_b32_e32 v9, v35
	v_lshlrev_b32_e32 v10, 2, v10
	v_mov_b32_e32 v11, v35
	v_lshlrev_b32_e32 v12, 2, v12
	v_mov_b32_e32 v13, v35
	v_mov_b32_e32 v17, v35
	v_mov_b32_e32 v19, v35
	v_mov_b32_e32 v21, v35
	v_mov_b32_e32 v23, v35
	v_mov_b32_e32 v25, v35
	v_mov_b32_e32 v27, v35
	v_mov_b32_e32 v29, v35
	v_mov_b32_e32 v31, v35
	v_mov_b32_e32 v43, v35
	v_mov_b32_e32 v45, v35
	v_lshl_add_u64 v[122:123], v[40:41], 0, v[76:77]
	v_lshlrev_b32_e32 v14, 2, v14
	v_mov_b32_e32 v15, v35
	v_bfe_u32 v76, v1, 3, 3
	v_lshlrev_b32_e32 v1, 3, v1
	v_lshl_add_u64 v[4:5], v[40:41], 0, v[4:5]
	v_lshl_add_u64 v[6:7], v[40:41], 0, v[6:7]
	v_lshl_add_u64 v[8:9], v[40:41], 0, v[8:9]
	v_lshl_add_u64 v[10:11], v[40:41], 0, v[10:11]
	v_lshl_add_u64 v[12:13], v[40:41], 0, v[12:13]
	v_lshl_add_u64 v[16:17], v[40:41], 0, v[16:17]
	v_lshl_add_u64 v[18:19], v[40:41], 0, v[18:19]
	v_lshl_add_u64 v[20:21], v[40:41], 0, v[20:21]
	v_lshl_add_u64 v[22:23], v[40:41], 0, v[22:23]
	v_lshl_add_u64 v[24:25], v[40:41], 0, v[24:25]
	v_lshl_add_u64 v[26:27], v[40:41], 0, v[26:27]
	v_lshl_add_u64 v[28:29], v[40:41], 0, v[28:29]
	v_lshl_add_u64 v[30:31], v[40:41], 0, v[30:31]
	v_lshl_add_u64 v[42:43], v[40:41], 0, v[42:43]
	v_lshl_add_u64 v[44:45], v[40:41], 0, v[44:45]
	v_lshl_add_u64 v[40:41], v[40:41], 0, v[14:15]
	v_and_b32_e32 v14, 56, v1
	v_mul_u32_u24_e32 v1, 0x84, v14
	v_lshlrev_b32_e32 v32, 2, v76
	v_add_u32_e32 v15, v3, v34
	v_add3_u32 v77, v3, v1, v32
	v_add_u32_e32 v3, s20, v39
	v_mov_b32_e32 v32, 0xfebc0000
	v_mul_u32_u24_e32 v1, 0x84, v33
	v_lshl_add_u32 v85, v3, 11, v32
	v_mov_b32_e32 v32, 0xffde0000
;     ...
;     const int I_E = it_hi < I_L ? it_hi : I_L;
;     int it = it_lo + gw;
;     if (it < I_E) { const PrepItem p = prep_decode(a, l, it);
; #pragma unroll
;         for (int i = 0; i < 32; ++i) tv[i] = __builtin_nontemporal_load(p.src + (size_t)(2 * i + (lane >> 5)) * p.ldw + (lane & 31)); }
	s_load_dwordx2 s[6:7], s[54:55], 0xa0
	s_load_dwordx2 s[8:9], s[54:55], 0x90
	s_load_dwordx2 s[16:17], s[54:55], 0x30
	s_load_dwordx2 s[18:19], s[54:55], 0x68
	v_lshlrev_b32_e32 v84, 3, v3
	v_lshl_add_u32 v86, v3, 10, v32
	v_lshlrev_b32_e32 v87, 4, v3
	v_add_u32_e32 v88, v15, v1
	v_lshlrev_b32_e32 v34, 2, v2
	v_lshlrev_b32_e32 v38, 1, v14
	global_load_dword v2, v[4:5], off
	global_load_dword v1, v[6:7], off
	s_nop 0
	global_load_dword v4, v[8:9], off
	global_load_dword v3, v[10:11], off
	global_load_dword v6, v[12:13], off
	global_load_dword v5, v[16:17], off
	s_nop 0
	global_load_dword v8, v[18:19], off
	global_load_dword v7, v[20:21], off
	global_load_dword v10, v[22:23], off
	global_load_dword v9, v[24:25], off
	global_load_dword v12, v[26:27], off
	global_load_dword v11, v[28:29], off
	global_load_dword v14, v[30:31], off
	global_load_dword v13, v[42:43], off
	global_load_dword v16, v[44:45], off
	global_load_dword v15, v[92:93], off
	global_load_dword v18, v[94:95], off
	global_load_dword v17, v[96:97], off
	global_load_dword v20, v[98:99], off
	global_load_dword v19, v[100:101], off
	global_load_dword v22, v[102:103], off
	global_load_dword v21, v[104:105], off
	global_load_dword v24, v[106:107], off
	global_load_dword v23, v[108:109], off
	global_load_dword v26, v[110:111], off
	global_load_dword v25, v[112:113], off
	global_load_dword v28, v[114:115], off
	global_load_dword v27, v[116:117], off
	global_load_dword v30, v[118:119], off
	global_load_dword v29, v[120:121], off
	global_load_dword v32, v[122:123], off
	global_load_dword v31, v[40:41], off
	s_waitcnt lgkmcnt(0)
	s_add_u32 s10, s6, 0x5b00000
	s_addc_u32 s11, s7, 0
	s_add_u32 s12, s6, 0x1b00000
	s_addc_u32 s13, s7, 0
	s_add_u32 s14, s6, 0xa00000
	v_or_b32_e32 v78, 8, v76
	v_or_b32_e32 v79, 16, v76
	v_or_b32_e32 v80, 24, v76
	s_addc_u32 s15, s7, 0
	v_lshlrev_b32_e32 v36, 5, v39
	s_lshl_b32 s2, s20, 5
	v_lshlrev_b32_e32 v81, 1, v39
	s_lshl_b32 s3, s20, 1
	v_lshlrev_b32_e32 v82, 15, v39
	s_lshl_b32 s34, s20, 15
	v_lshlrev_b32_e32 v83, 16, v39
	s_lshl_b32 s35, s20, 16
	s_lshl_b32 s38, s20, 3
	s_lshl_b32 s39, s20, 11
	s_lshl_b32 s40, s20, 10
	s_lshl_b32 s41, s20, 4
	s_mov_b64 s[20:21], 0
	s_movk_i32 s42, 0x67f
	s_movk_i32 s43, 0x87f
	s_movk_i32 s44, 0x287f
	s_mov_b64 s[22:23], 0x16fe600
	s_mov_b32 s45, 0x4ec4ec4f
	s_movk_i32 s46, 0xf300
	s_movk_i32 s47, 0x3880
	s_movk_i32 s48, 0x387f
	s_movk_i32 s49, 0xff98
	s_mov_b32 s50, 0xd0400
	v_mov_b32_e32 v89, 0x88
	v_mov_b32_e32 v90, 0x80
	s_branch .LBB0_31
;     ...
;     for (; it < I_E; it += ngw) {
;         const PrepItem p = prep_decode(a, l, it);
; #pragma unroll
;         for (int i = 0; i < 32; ++i) scr[(2 * i + (lane >> 5)) * 33 + (lane & 31)] = tv[i];
;         if (it + ngw < I_E) { const PrepItem q = prep_decode(a, l, it + ngw);
; #pragma unroll
;             for (int i = 0; i < 32; ++i) tv[i] = __builtin_nontemporal_load(q.src + (size_t)(2 * i + (lane >> 5)) * q.ldw + (lane & 31)); }
.LBB0_29:
	s_or_b64 exec, exec, s[26:27]
	v_mul_u32_u24_e32 v1, v2, v33
	v_lshlrev_b32_e32 v6, 2, v1
	v_mul_u32_u24_e32 v1, v2, v37
	v_lshlrev_b32_e32 v8, 2, v1
	v_mul_u32_u24_e32 v1, v2, v46
	v_lshlrev_b32_e32 v10, 2, v1
	v_mul_u32_u24_e32 v1, v2, v47
	v_lshlrev_b32_e32 v12, 2, v1
	v_mul_u32_u24_e32 v1, v2, v48
	v_lshlrev_b32_e32 v14, 2, v1
	v_mul_u32_u24_e32 v1, v2, v49
	v_lshlrev_b32_e32 v16, 2, v1
	v_mul_u32_u24_e32 v1, v2, v50
	v_lshlrev_b32_e32 v18, 2, v1
	v_mul_u32_u24_e32 v1, v2, v51
	v_lshlrev_b32_e32 v20, 2, v1
	v_mul_u32_u24_e32 v1, v2, v52
	v_lshlrev_b32_e32 v22, 2, v1
	v_mul_u32_u24_e32 v1, v2, v53
	v_lshlrev_b32_e32 v24, 2, v1
	v_mul_u32_u24_e32 v1, v2, v54
	v_lshlrev_b32_e32 v26, 2, v1
	v_mul_u32_u24_e32 v1, v2, v55
	v_lshlrev_b32_e32 v28, 2, v1
	v_mul_u32_u24_e32 v1, v2, v56
	v_lshlrev_b32_e32 v30, 2, v1
	v_mul_u32_u24_e32 v1, v2, v57
	v_lshlrev_b32_e32 v92, 2, v1
	v_mul_u32_u24_e32 v1, v2, v58
	v_lshlrev_b32_e32 v94, 2, v1
	v_mul_u32_u24_e32 v1, v2, v59
	v_lshlrev_b32_e32 v96, 2, v1
	v_mul_u32_u24_e32 v1, v2, v60
	v_lshlrev_b32_e32 v98, 2, v1
	v_mul_u32_u24_e32 v1, v2, v61
	v_lshlrev_b32_e32 v100, 2, v1
	v_mul_u32_u24_e32 v1, v2, v62
	v_lshlrev_b32_e32 v102, 2, v1
	v_mul_u32_u24_e32 v1, v2, v63
	v_lshlrev_b32_e32 v104, 2, v1
	v_mul_u32_u24_e32 v1, v2, v64
	v_lshlrev_b32_e32 v106, 2, v1
	v_mul_u32_u24_e32 v1, v2, v65
	v_lshlrev_b32_e32 v108, 2, v1
	v_mul_u32_u24_e32 v1, v2, v66
	v_lshlrev_b32_e32 v110, 2, v1
	v_mul_u32_u24_e32 v1, v2, v67
	v_lshlrev_b32_e32 v112, 2, v1
	v_mul_u32_u24_e32 v1, v2, v68
	v_lshlrev_b32_e32 v114, 2, v1
	v_mul_u32_u24_e32 v1, v2, v69
	v_lshlrev_b32_e32 v116, 2, v1
	v_mul_u32_u24_e32 v1, v2, v70
	v_lshlrev_b32_e32 v118, 2, v1
	v_mul_u32_u24_e32 v1, v2, v71
	v_lshlrev_b32_e32 v120, 2, v1
	v_mul_u32_u24_e32 v1, v2, v72
	v_lshlrev_b32_e32 v122, 2, v1
	v_mul_u32_u24_e32 v1, v2, v73
	v_lshlrev_b32_e32 v124, 2, v1
	v_mul_u32_u24_e32 v1, v2, v74
	v_lshl_add_u64 v[4:5], v[4:5], 0, v[34:35]
	v_mov_b32_e32 v7, v35
	v_mov_b32_e32 v9, v35
	v_mov_b32_e32 v11, v35
	v_mov_b32_e32 v13, v35
	v_mov_b32_e32 v15, v35
	v_mov_b32_e32 v17, v35
	v_mov_b32_e32 v19, v35
	v_mov_b32_e32 v21, v35
	v_mov_b32_e32 v23, v35
	v_mov_b32_e32 v25, v35
	v_mov_b32_e32 v27, v35
	v_mov_b32_e32 v29, v35
	v_mov_b32_e32 v31, v35
	v_lshlrev_b32_e32 v126, 2, v1
	v_mul_u32_u24_e32 v1, v2, v75
	v_lshl_add_u64 v[6:7], v[4:5], 0, v[6:7]
	v_lshl_add_u64 v[8:9], v[4:5], 0, v[8:9]
	v_lshl_add_u64 v[10:11], v[4:5], 0, v[10:11]
	v_lshl_add_u64 v[12:13], v[4:5], 0, v[12:13]
	v_lshl_add_u64 v[14:15], v[4:5], 0, v[14:15]
	v_lshl_add_u64 v[16:17], v[4:5], 0, v[16:17]
	v_lshl_add_u64 v[18:19], v[4:5], 0, v[18:19]
	v_lshl_add_u64 v[20:21], v[4:5], 0, v[20:21]
	v_lshl_add_u64 v[22:23], v[4:5], 0, v[22:23]
	v_lshl_add_u64 v[24:25], v[4:5], 0, v[24:25]
	v_lshl_add_u64 v[26:27], v[4:5], 0, v[26:27]
	v_lshl_add_u64 v[28:29], v[4:5], 0, v[28:29]
	v_lshl_add_u64 v[30:31], v[4:5], 0, v[30:31]
	v_mov_b32_e32 v93, v35
	v_mov_b32_e32 v95, v35
	v_mov_b32_e32 v97, v35
	v_mov_b32_e32 v99, v35
	v_mov_b32_e32 v101, v35
	v_mov_b32_e32 v103, v35
	v_mov_b32_e32 v105, v35
	v_mov_b32_e32 v107, v35
	v_mov_b32_e32 v109, v35
	v_mov_b32_e32 v111, v35
	v_mov_b32_e32 v113, v35
	v_mov_b32_e32 v115, v35
	v_mov_b32_e32 v117, v35
	v_mov_b32_e32 v119, v35
	v_mov_b32_e32 v121, v35
	v_mov_b32_e32 v123, v35
	v_mov_b32_e32 v125, v35
	v_mov_b32_e32 v127, v35
	v_lshlrev_b32_e32 v2, 2, v1
	v_mov_b32_e32 v3, v35
	v_lshl_add_u64 v[92:93], v[4:5], 0, v[92:93]
	v_lshl_add_u64 v[94:95], v[4:5], 0, v[94:95]
	v_lshl_add_u64 v[96:97], v[4:5], 0, v[96:97]
	v_lshl_add_u64 v[98:99], v[4:5], 0, v[98:99]
	v_lshl_add_u64 v[100:101], v[4:5], 0, v[100:101]
	v_lshl_add_u64 v[102:103], v[4:5], 0, v[102:103]
	v_lshl_add_u64 v[104:105], v[4:5], 0, v[104:105]
	v_lshl_add_u64 v[106:107], v[4:5], 0, v[106:107]
	v_lshl_add_u64 v[108:109], v[4:5], 0, v[108:109]
	v_lshl_add_u64 v[110:111], v[4:5], 0, v[110:111]
	v_lshl_add_u64 v[112:113], v[4:5], 0, v[112:113]
	v_lshl_add_u64 v[114:115], v[4:5], 0, v[114:115]
	v_lshl_add_u64 v[116:117], v[4:5], 0, v[116:117]
	v_lshl_add_u64 v[118:119], v[4:5], 0, v[118:119]
	v_lshl_add_u64 v[120:121], v[4:5], 0, v[120:121]
	v_lshl_add_u64 v[122:123], v[4:5], 0, v[122:123]
	v_lshl_add_u64 v[124:125], v[4:5], 0, v[124:125]
	v_lshl_add_u64 v[126:127], v[4:5], 0, v[126:127]
	v_lshl_add_u64 v[128:129], v[4:5], 0, v[2:3]
	global_load_dword v2, v[6:7], off
	global_load_dword v1, v[8:9], off
	global_load_dword v4, v[10:11], off
	global_load_dword v3, v[12:13], off
	s_nop 0
	global_load_dword v6, v[14:15], off
	global_load_dword v5, v[16:17], off
	global_load_dword v8, v[18:19], off
	global_load_dword v7, v[20:21], off
	global_load_dword v10, v[22:23], off
	global_load_dword v9, v[24:25], off
	global_load_dword v12, v[26:27], off
	global_load_dword v11, v[28:29], off
	global_load_dword v14, v[30:31], off
	global_load_dword v13, v[92:93], off
	global_load_dword v16, v[94:95], off
	global_load_dword v15, v[96:97], off
	global_load_dword v18, v[98:99], off
	global_load_dword v17, v[100:101], off
	global_load_dword v20, v[102:103], off
	global_load_dword v19, v[104:105], off
	global_load_dword v22, v[106:107], off
	global_load_dword v21, v[108:109], off
	global_load_dword v24, v[110:111], off
	global_load_dword v23, v[112:113], off
	global_load_dword v26, v[114:115], off
	global_load_dword v25, v[116:117], off
	global_load_dword v28, v[118:119], off
	global_load_dword v27, v[120:121], off
	global_load_dword v30, v[122:123], off
	global_load_dword v29, v[124:125], off
	global_load_dword v32, v[126:127], off
	global_load_dword v31, v[128:129], off

; __device__ __forceinline__ void n1_norm(const Args& a, LAS unsigned char* lds, int layer, bool dry = false) {
;     ...
;         const int row0 = rg * 16, b = row0 / S;
;         const float* sh = mod + ((size_t)layer * NB + b) * 6144;
;         const float* sc = sh + 1024;
;         const float* gf = mod + ((size_t)(layer > 0 ? layer - 1 : 0) * NB + b) * 6144 + 5120;
;         f32x4 ga[4], s0v[4], gfv[4];
; #pragma unroll
;         for (int j = 0; j < 4; ++j) { const int col = 8 * lane + 512 * (j >> 1) + 4 * (j & 1);
;             ga[j] = *(const f32x4*)(nm + col) * (1.f + *(const f32x4*)(sc + col)); s0v[j] = *(const f32x4*)(sh + col); gfv[j] = *(const f32x4*)(gf + col); }
;         u32x4 nb[2][6];
;     ...
;         N1_LOAD(0, row0); N1_LOAD(1, row0 + 1);
.LBB0_106:
	v_ashrrev_i32_e32 v34, 31, v189
	v_add_u32_sdwa v34, v189, v34 dst_sel:DWORD dst_unused:UNUSED_PAD src0_sel:DWORD src1_sel:BYTE_3
	v_ashrrev_i32_e32 v68, 8, v34
	v_readlane_b32 s18, v252, 12
	v_ashrrev_i32_e32 v69, 31, v68
	v_readlane_b32 s19, v252, 13
	v_lshl_add_u64 v[70:71], s[14:15], 0, v[68:69]
	s_movk_i32 s2, 0x6000
	v_mov_b64_e32 v[72:73], s[18:19]
	v_mad_u64_u32 v[72:73], s[10:11], v70, s2, v[72:73]
	v_mad_i32_i24 v73, v71, s2, v73
	s_mov_b64 s[10:11], 0x1000
	v_mul_hi_i32_i24_e32 v69, 0x6000, v68
	v_mul_i32_i24_e32 v68, 0x6000, v68
	v_lshl_add_u64 v[84:85], v[72:73], 0, s[10:11]
	v_lshl_add_u64 v[68:69], s[18:19], 0, v[68:69]
	s_mov_b64 s[10:11], 0x5000
	v_lshl_add_u64 v[92:93], v[68:69], 0, s[10:11]
	v_lshlrev_b32_e32 v34, 2, v188
	v_mov_b32_e32 v209, v35
	v_lshl_add_u64 v[68:69], v[84:85], 0, v[34:35]
	v_lshl_add_u64 v[88:89], v[72:73], 0, v[34:35]
	v_lshl_add_u64 v[80:81], v[92:93], 0, v[34:35]
	v_lshl_add_u64 v[84:85], v[84:85], 0, v[208:209]
	global_load_dwordx4 v[124:127], v[194:195], off offset:16
	global_load_dwordx4 v[128:131], v[194:195], off
	global_load_dwordx4 v[136:139], v[68:69], off offset:16
	s_waitcnt lgkmcnt(0)
	global_load_dwordx4 v[164:167], v[68:69], off
	s_nop 0
	global_load_dwordx4 v[68:71], v[88:89], off offset:16
	global_load_dwordx4 v[72:75], v[88:89], off
	global_load_dwordx4 v[76:79], v[80:81], off offset:16
	s_nop 0
	global_load_dwordx4 v[80:83], v[80:81], off
	s_nop 0
	global_load_dwordx4 v[132:135], v[194:195], off offset:2064
	global_load_dwordx4 v[156:159], v[194:195], off offset:2048
	global_load_dwordx4 v[160:163], v[84:85], off offset:16
	global_load_dwordx4 v[168:171], v[84:85], off
	s_nop 0
	global_load_dwordx4 v[84:87], v[88:89], off offset:2064
	s_nop 0
	global_load_dwordx4 v[88:91], v[88:89], off offset:2048
	v_lshl_add_u64 v[96:97], v[92:93], 0, v[208:209]
	global_load_dwordx4 v[92:95], v[96:97], off offset:16
	s_nop 0
	global_load_dwordx4 v[96:99], v[96:97], off
	v_readlane_b32 s18, v254, 16
	v_readlane_b32 s19, v254, 17
	v_lshlrev_b32_e32 v172, 4, v189
	v_ashrrev_i32_e32 v173, 31, v172
	v_cndmask_b32_e64 v34, 0, 1, s[18:19]
	v_cmp_ne_u32_e64 s[10:11], 1, v34
	s_andn2_b64 vcc, exec, s[18:19]
	s_mov_b64 s[18:19], -1
	s_cbranch_vccnz .LBB0_108
	v_lshlrev_b64 v[102:103], 11, v[172:173]
	v_lshl_or_b32 v102, v188, 1, v102
	v_lshl_add_u64 v[100:101], s[50:51], 0, v[102:103]
	v_lshl_add_u64 v[104:105], s[96:97], 0, v[102:103]
	v_lshl_add_u64 v[116:117], s[0:1], 0, v[102:103]
	v_or_b32_e32 v102, 0x400, v102
	v_lshl_add_u64 v[106:107], s[96:97], 0, v[102:103]
	v_lshl_add_u64 v[118:119], s[0:1], 0, v[102:103]
	global_load_dwordx4 v[152:155], v[106:107], off
	global_load_dwordx4 v[148:151], v[118:119], off
	v_lshl_add_u64 v[120:121], s[50:51], 0, v[102:103]
	s_mov_b64 s[18:19], 0

; __device__ __forceinline__ void n1_norm(const Args& a, LAS unsigned char* lds, int layer, bool dry = false) {
;     ...
;         N1_LOAD(0, row0); N1_LOAD(1, row0 + 1);
.LBB0_110:
	global_load_dwordx4 v[100:103], v[100:101], off
	s_nop 0
	global_load_dwordx4 v[104:107], v[104:105], off
	s_nop 0
	global_load_dwordx4 v[116:119], v[116:117], off
	s_nop 0
	global_load_dwordx4 v[120:123], v[120:121], off
	v_or_b32_e32 v180, 1, v172
	v_ashrrev_i32_e32 v181, 31, v180
	s_and_b64 vcc, exec, s[10:11]
	s_mov_b64 s[18:19], -1
	s_cbranch_vccnz .LBB0_112
	v_lshlrev_b64 v[178:179], 11, v[180:181]
	v_lshl_or_b32 v178, v188, 1, v178
	v_lshl_add_u64 v[172:173], s[50:51], 0, v[178:179]
	v_lshl_add_u64 v[174:175], s[96:97], 0, v[178:179]
	v_lshl_add_u64 v[176:177], s[0:1], 0, v[178:179]
	v_or_b32_e32 v178, 0x400, v178
	v_lshl_add_u64 v[140:141], s[96:97], 0, v[178:179]
	v_lshl_add_u64 v[144:145], s[0:1], 0, v[178:179]
	global_load_dwordx4 v[140:143], v[140:141], off
	s_nop 0
	global_load_dwordx4 v[144:147], v[144:145], off
	v_lshl_add_u64 v[178:179], s[50:51], 0, v[178:179]
	s_mov_b64 s[18:19], 0

; __device__ __forceinline__ void n1_norm(const Args& a, LAS unsigned char* lds, int layer, bool dry = false) {
;     ...
;         for (int j = 0; j < 4; ++j) { const int col = 8 * lane + 512 * (j >> 1) + 4 * (j & 1);
;             ga[j] = *(const f32x4*)(nm + col) * (1.f + *(const f32x4*)(sc + col)); s0v[j] = *(const f32x4*)(sh + col); gfv[j] = *(const f32x4*)(gf + col); }
;         u32x4 nb[2][6];
;     ...
;         N1_LOAD(0, row0); N1_LOAD(1, row0 + 1);
.LBB0_114:
	s_waitcnt vmcnt(16)
	v_pk_add_f32 v[108:109], v[166:167], 1.0 op_sel_hi:[1,0]
	v_pk_add_f32 v[110:111], v[164:165], 1.0 op_sel_hi:[1,0]
	v_pk_mul_f32 v[210:211], v[130:131], v[108:109]
	v_pk_mul_f32 v[212:213], v[128:129], v[110:111]
	v_pk_add_f32 v[108:109], v[136:137], 1.0 op_sel_hi:[1,0]
	v_pk_add_f32 v[110:111], v[138:139], 1.0 op_sel_hi:[1,0]
	v_pk_mul_f32 v[216:217], v[124:125], v[108:109]
	v_pk_mul_f32 v[214:215], v[126:127], v[110:111]
	s_waitcnt vmcnt(8)
	v_pk_add_f32 v[108:109], v[170:171], 1.0 op_sel_hi:[1,0]
	v_pk_add_f32 v[110:111], v[168:169], 1.0 op_sel_hi:[1,0]
	v_pk_mul_f32 v[218:219], v[158:159], v[108:109]
	v_pk_mul_f32 v[220:221], v[156:157], v[110:111]
	v_pk_add_f32 v[108:109], v[160:161], 1.0 op_sel_hi:[1,0]
	v_pk_add_f32 v[110:111], v[162:163], 1.0 op_sel_hi:[1,0]
	v_pk_mul_f32 v[224:225], v[132:133], v[108:109]
	v_pk_mul_f32 v[222:223], v[134:135], v[110:111]
	global_load_dwordx4 v[124:127], v[172:173], off
	global_load_dwordx4 v[128:131], v[174:175], off
	global_load_dwordx4 v[132:135], v[176:177], off
	global_load_dwordx4 v[136:139], v[178:179], off
	s_waitcnt vmcnt(4)
	v_mov_b64_e32 v[108:109], v[144:145]
	v_mov_b64_e32 v[112:113], v[140:141]
	s_mov_b32 s2, 0
	v_mov_b64_e32 v[110:111], v[146:147]
	v_mov_b64_e32 v[114:115], v[142:143]
	s_and_b64 vcc, exec, s[10:11]
	s_cbranch_vccnz .LBB0_116
	s_branch .LBB0_118

; __device__ __forceinline__ f32x4 bf4_lo(const u32x4& v) { return (f32x4){__uint_as_float(v.x << 16), __uint_as_float(v.x & 0xffff0000u), __uint_as_float(v.y << 16), __uint_as_float(v.y & 0xffff0000u)}; }
; __device__ __forceinline__ f32x4 bf4_hi(const u32x4& v) { return (f32x4){__uint_as_float(v.z << 16), __uint_as_float(v.z & 0xffff0000u), __uint_as_float(v.w << 16), __uint_as_float(v.w & 0xffff0000u)}; }
; __device__ __forceinline__ void n1_norm(const Args& a, LAS unsigned char* lds, int layer, bool dry = false) {
;     ...
;         N1_LOAD(0, row0); N1_LOAD(1, row0 + 1);
; #pragma unroll 1
;         for (int i = 0; i < 16; i += 2) {
;             f32x4 v[2][4];
; #pragma unroll
;             for (int q2 = 0; q2 < 2; ++q2) {
;                 if (layer == 0) {
; #pragma unroll
;                     for (int j = 0; j < 4; ++j) v[q2][j] = __builtin_bit_cast(f32x4, nb[q2][j]);
;                 } else {
; #pragma unroll
;                     for (int jp = 0; jp < 2; ++jp) {
;                         v[q2][2 * jp] = bf4_lo(nb[q2][3 * jp]) + gfv[2 * jp] * (bf4_lo(nb[q2][3 * jp + 1]) + bf4_lo(nb[q2][3 * jp + 2]));
;                         v[q2][2 * jp + 1] = bf4_hi(nb[q2][3 * jp]) + gfv[2 * jp + 1] * (bf4_hi(nb[q2][3 * jp + 1]) + bf4_hi(nb[q2][3 * jp + 2]));
;                     }
;                 }
;             }
;             if (i < 14) { N1_LOAD(0, row0 + i + 2); N1_LOAD(1, row0 + i + 3); }
.LBB0_122:
	s_andn2_b64 vcc, exec, s[20:21]
	s_cbranch_vccnz .LBB0_132
	v_add_u32_e32 v102, 2, v226
	v_ashrrev_i32_e32 v103, 31, v102
	s_and_b64 vcc, exec, s[10:11]
	s_mov_b64 s[20:21], -1
	s_cbranch_vccnz .LBB0_125
	v_lshlrev_b64 v[106:107], 11, v[102:103]
	v_lshl_or_b32 v106, v188, 1, v106
	v_lshl_add_u64 v[100:101], s[50:51], 0, v[106:107]
	v_lshl_add_u64 v[104:105], s[96:97], 0, v[106:107]
	v_lshl_add_u64 v[116:117], s[0:1], 0, v[106:107]
	v_or_b32_e32 v106, 0x400, v106
	v_lshl_add_u64 v[118:119], s[96:97], 0, v[106:107]
	v_lshl_add_u64 v[120:121], s[0:1], 0, v[106:107]
	global_load_dwordx4 v[140:143], v[118:119], off
	global_load_dwordx4 v[144:147], v[120:121], off
	v_lshl_add_u64 v[120:121], s[50:51], 0, v[106:107]
	s_mov_b64 s[20:21], 0

; __device__ __forceinline__ f32x4 bf4_lo(const u32x4& v) { return (f32x4){__uint_as_float(v.x << 16), __uint_as_float(v.x & 0xffff0000u), __uint_as_float(v.y << 16), __uint_as_float(v.y & 0xffff0000u)}; }
; __device__ __forceinline__ f32x4 bf4_hi(const u32x4& v) { return (f32x4){__uint_as_float(v.z << 16), __uint_as_float(v.z & 0xffff0000u), __uint_as_float(v.w << 16), __uint_as_float(v.w & 0xffff0000u)}; }
; __device__ __forceinline__ void n1_norm(const Args& a, LAS unsigned char* lds, int layer, bool dry = false) {
;     ...
;         N1_LOAD(0, row0); N1_LOAD(1, row0 + 1);
; #pragma unroll 1
;         for (int i = 0; i < 16; i += 2) {
;             f32x4 v[2][4];
; #pragma unroll
;             for (int q2 = 0; q2 < 2; ++q2) {
;                 if (layer == 0) {
; #pragma unroll
;                     for (int j = 0; j < 4; ++j) v[q2][j] = __builtin_bit_cast(f32x4, nb[q2][j]);
;                 } else {
; #pragma unroll
;                     for (int jp = 0; jp < 2; ++jp) {
;                         v[q2][2 * jp] = bf4_lo(nb[q2][3 * jp]) + gfv[2 * jp] * (bf4_lo(nb[q2][3 * jp + 1]) + bf4_lo(nb[q2][3 * jp + 2]));
;                         v[q2][2 * jp + 1] = bf4_hi(nb[q2][3 * jp]) + gfv[2 * jp + 1] * (bf4_hi(nb[q2][3 * jp + 1]) + bf4_hi(nb[q2][3 * jp + 2]));
;                     }
;                 }
;             }
;             if (i < 14) { N1_LOAD(0, row0 + i + 2); N1_LOAD(1, row0 + i + 3); }
.LBB0_127:
	global_load_dwordx4 v[100:103], v[100:101], off
	s_nop 0
	global_load_dwordx4 v[104:107], v[104:105], off
	s_nop 0
	global_load_dwordx4 v[116:119], v[116:117], off
	s_nop 0
	global_load_dwordx4 v[120:123], v[120:121], off
	v_add_u32_e32 v228, 3, v226
	v_ashrrev_i32_e32 v229, 31, v228
	s_and_b64 vcc, exec, s[10:11]
	s_mov_b64 s[20:21], -1
	s_cbranch_vccnz .LBB0_129
	v_lshlrev_b64 v[148:149], 11, v[228:229]
	v_lshl_or_b32 v148, v188, 1, v148
	v_lshl_add_u64 v[124:125], s[50:51], 0, v[148:149]
	v_lshl_add_u64 v[128:129], s[96:97], 0, v[148:149]
	v_lshl_add_u64 v[132:133], s[0:1], 0, v[148:149]
	v_or_b32_e32 v148, 0x400, v148
	v_lshl_add_u64 v[136:137], s[50:51], 0, v[148:149]
	v_lshl_add_u64 v[150:151], s[96:97], 0, v[148:149]
	v_lshl_add_u64 v[152:153], s[0:1], 0, v[148:149]
	global_load_dwordx4 v[124:127], v[124:125], off
	s_nop 0
	global_load_dwordx4 v[128:131], v[128:129], off
	s_nop 0
	global_load_dwordx4 v[132:135], v[132:133], off
	s_nop 0
	global_load_dwordx4 v[136:139], v[136:137], off
	s_nop 0
	global_load_dwordx4 v[148:151], v[150:151], off
	s_nop 0
	global_load_dwordx4 v[152:155], v[152:153], off
	s_mov_b64 s[20:21], 0
.LBB0_129:
	s_andn2_b64 vcc, exec, s[20:21]
	s_cbranch_vccnz .LBB0_131
	s_waitcnt vmcnt(5)
	v_lshlrev_b64 v[124:125], 12, v[228:229]
	s_waitcnt vmcnt(3)
	v_lshl_add_u64 v[132:133], v[196:197], 0, v[124:125]
	global_load_dwordx4 v[128:131], v[132:133], off offset:16
	global_load_dwordx4 v[124:127], v[132:133], off
	global_load_dwordx4 v[136:139], v[132:133], off offset:2064
	s_nop 0
	global_load_dwordx4 v[132:135], v[132:133], off offset:2048
	s_waitcnt vmcnt(5)
	v_mov_b64_e32 v[150:151], v[114:115]
	s_waitcnt vmcnt(4)
	v_mov_b64_e32 v[154:155], v[110:111]
	v_mov_b64_e32 v[148:149], v[112:113]
	v_mov_b64_e32 v[152:153], v[108:109]

; #define LAS __attribute__((address_space(3)))
;     ...
;     LAS float* scr = (LAS float*)(lds + 49152) + wave * (64 * 33);
;     const int gw = ((int)blockIdx.x - blk0) * NWAVES + wave, ngw = nblk * NWAVES;
;     constexpr int I_L = 16 * 104 + 16 * 32 + 16 * 16 * 32 + 16 * 8 * 32;
;     if ((int)blockIdx.x < blk0 || (int)blockIdx.x >= blk0 + nblk) return;
;     float tv[32];
;     const int I_E = it_hi < I_L ? it_hi : I_L;
;     int it = it_lo + gw;
;     if (it < I_E) { const PrepItem p = prep_decode(a, l, it);
; #pragma unroll
;         for (int i = 0; i < 32; ++i) tv[i] = __builtin_nontemporal_load(p.src + (size_t)(2 * i + (lane >> 5)) * p.ldw + (lane & 31)); }
.LBB0_317:
	s_or_b64 exec, exec, s[4:5]
	s_movk_i32 s2, 0x2100
	v_mul_lo_u32 v1, v1, s2
	v_and_b32_e32 v36, 31, v42
	v_bfe_u32 v33, v42, 5, 1
	v_add_u32_e32 v43, 0, v1
	v_lshlrev_b32_e32 v34, 2, v36
	v_mul_u32_u24_e32 v1, v38, v33
	v_or_b32_e32 v48, 2, v33
	v_lshl_add_u64 v[40:41], v[2:3], 0, v[34:35]
	v_lshlrev_b32_e32 v2, 2, v1
	v_mul_u32_u24_e32 v1, v38, v48
	v_mov_b32_e32 v3, v35
	v_lshlrev_b32_e32 v4, 2, v1
	v_mov_b32_e32 v5, v35
	v_lshl_add_u64 v[2:3], v[40:41], 0, v[2:3]
	v_lshl_add_u64 v[4:5], v[40:41], 0, v[4:5]
	v_or_b32_e32 v49, 4, v33
	global_load_dword v2, v[2:3], off
	v_or_b32_e32 v50, 6, v33
	global_load_dword v1, v[4:5], off
	v_mul_u32_u24_e32 v3, v38, v49
	v_lshlrev_b32_e32 v4, 2, v3
	v_mul_u32_u24_e32 v3, v38, v50
	v_mov_b32_e32 v5, v35
	v_lshlrev_b32_e32 v6, 2, v3
	v_mov_b32_e32 v7, v35
	v_lshl_add_u64 v[4:5], v[40:41], 0, v[4:5]
	v_lshl_add_u64 v[6:7], v[40:41], 0, v[6:7]
	v_or_b32_e32 v51, 8, v33
	global_load_dword v4, v[4:5], off
	v_or_b32_e32 v52, 10, v33
	global_load_dword v3, v[6:7], off
	v_mul_u32_u24_e32 v5, v38, v51
	v_lshlrev_b32_e32 v6, 2, v5
	v_mul_u32_u24_e32 v5, v38, v52
	v_mov_b32_e32 v7, v35
	v_lshlrev_b32_e32 v8, 2, v5
	v_mov_b32_e32 v9, v35
	v_lshl_add_u64 v[6:7], v[40:41], 0, v[6:7]
	v_lshl_add_u64 v[8:9], v[40:41], 0, v[8:9]
	v_or_b32_e32 v53, 12, v33
	global_load_dword v6, v[6:7], off
	v_or_b32_e32 v54, 14, v33
	global_load_dword v5, v[8:9], off
	v_mul_u32_u24_e32 v7, v38, v53
	v_lshlrev_b32_e32 v8, 2, v7
	v_mul_u32_u24_e32 v7, v38, v54
	v_mov_b32_e32 v9, v35
	v_lshlrev_b32_e32 v10, 2, v7
	v_mov_b32_e32 v11, v35
	v_lshl_add_u64 v[8:9], v[40:41], 0, v[8:9]
	v_lshl_add_u64 v[10:11], v[40:41], 0, v[10:11]
	v_or_b32_e32 v55, 16, v33
	global_load_dword v8, v[8:9], off
	v_or_b32_e32 v56, 18, v33
	global_load_dword v7, v[10:11], off
	v_mul_u32_u24_e32 v9, v38, v55
	v_lshlrev_b32_e32 v10, 2, v9
	v_mul_u32_u24_e32 v9, v38, v56
	v_mov_b32_e32 v11, v35
	v_lshlrev_b32_e32 v12, 2, v9
	v_mov_b32_e32 v13, v35
	v_lshl_add_u64 v[10:11], v[40:41], 0, v[10:11]
	v_lshl_add_u64 v[12:13], v[40:41], 0, v[12:13]
	v_or_b32_e32 v57, 20, v33
	global_load_dword v10, v[10:11], off
	v_or_b32_e32 v58, 22, v33
	global_load_dword v9, v[12:13], off
	v_mul_u32_u24_e32 v11, v38, v57
	v_lshlrev_b32_e32 v12, 2, v11
	v_mul_u32_u24_e32 v11, v38, v58
	v_mov_b32_e32 v13, v35
	v_lshlrev_b32_e32 v14, 2, v11
	v_mov_b32_e32 v15, v35
	v_lshl_add_u64 v[12:13], v[40:41], 0, v[12:13]
	v_lshl_add_u64 v[14:15], v[40:41], 0, v[14:15]
	v_or_b32_e32 v59, 24, v33
	global_load_dword v12, v[12:13], off
	v_or_b32_e32 v60, 26, v33
	global_load_dword v11, v[14:15], off
	v_mul_u32_u24_e32 v13, v38, v59
	v_lshlrev_b32_e32 v14, 2, v13
	v_mul_u32_u24_e32 v13, v38, v60
	v_mov_b32_e32 v15, v35
	v_lshlrev_b32_e32 v16, 2, v13
	v_mov_b32_e32 v17, v35
	v_lshl_add_u64 v[14:15], v[40:41], 0, v[14:15]
	v_lshl_add_u64 v[16:17], v[40:41], 0, v[16:17]
	v_or_b32_e32 v61, 28, v33
	global_load_dword v14, v[14:15], off
	v_or_b32_e32 v62, 30, v33
	global_load_dword v13, v[16:17], off
	v_mul_u32_u24_e32 v15, v38, v61
	v_lshlrev_b32_e32 v16, 2, v15
	v_mul_u32_u24_e32 v15, v38, v62
	v_mov_b32_e32 v17, v35
	v_lshlrev_b32_e32 v18, 2, v15
	v_mov_b32_e32 v19, v35
	v_lshl_add_u64 v[16:17], v[40:41], 0, v[16:17]
	v_lshl_add_u64 v[18:19], v[40:41], 0, v[18:19]
	v_or_b32_e32 v63, 32, v33
	global_load_dword v16, v[16:17], off
	v_or_b32_e32 v64, 34, v33
	global_load_dword v15, v[18:19], off
	v_mul_u32_u24_e32 v17, v38, v63
	v_lshlrev_b32_e32 v18, 2, v17
	v_mul_u32_u24_e32 v17, v38, v64
	v_mov_b32_e32 v19, v35
	v_lshlrev_b32_e32 v20, 2, v17
	v_mov_b32_e32 v21, v35
	v_lshl_add_u64 v[18:19], v[40:41], 0, v[18:19]
	v_lshl_add_u64 v[20:21], v[40:41], 0, v[20:21]
	v_or_b32_e32 v65, 36, v33
	global_load_dword v18, v[18:19], off
	v_or_b32_e32 v66, 38, v33
	global_load_dword v17, v[20:21], off
	v_mul_u32_u24_e32 v19, v38, v65
	v_lshlrev_b32_e32 v20, 2, v19
	v_mul_u32_u24_e32 v19, v38, v66
	v_mov_b32_e32 v21, v35
	v_lshlrev_b32_e32 v22, 2, v19
	v_mov_b32_e32 v23, v35
	v_lshl_add_u64 v[20:21], v[40:41], 0, v[20:21]
	v_lshl_add_u64 v[22:23], v[40:41], 0, v[22:23]
	v_or_b32_e32 v67, 40, v33
	global_load_dword v20, v[20:21], off
	v_or_b32_e32 v68, 42, v33
	global_load_dword v19, v[22:23], off
	v_mul_u32_u24_e32 v21, v38, v67
	v_lshlrev_b32_e32 v22, 2, v21
	v_mul_u32_u24_e32 v21, v38, v68
	v_mov_b32_e32 v23, v35
	v_lshlrev_b32_e32 v24, 2, v21
	v_mov_b32_e32 v25, v35
	v_lshl_add_u64 v[22:23], v[40:41], 0, v[22:23]
	v_lshl_add_u64 v[24:25], v[40:41], 0, v[24:25]
	v_or_b32_e32 v69, 44, v33
	global_load_dword v22, v[22:23], off
	v_or_b32_e32 v70, 46, v33
	global_load_dword v21, v[24:25], off
	v_mul_u32_u24_e32 v23, v38, v69
	v_lshlrev_b32_e32 v24, 2, v23
	v_mul_u32_u24_e32 v23, v38, v70
	v_mov_b32_e32 v25, v35
	v_lshlrev_b32_e32 v26, 2, v23
	v_mov_b32_e32 v27, v35
	v_lshl_add_u64 v[24:25], v[40:41], 0, v[24:25]
	v_lshl_add_u64 v[26:27], v[40:41], 0, v[26:27]
	v_or_b32_e32 v71, 48, v33
	global_load_dword v24, v[24:25], off
	v_or_b32_e32 v72, 50, v33
	global_load_dword v23, v[26:27], off
	v_mul_u32_u24_e32 v25, v38, v71
	v_lshlrev_b32_e32 v26, 2, v25
	v_mul_u32_u24_e32 v25, v38, v72
	v_mov_b32_e32 v27, v35
	v_lshlrev_b32_e32 v28, 2, v25
	v_mov_b32_e32 v29, v35
	v_lshl_add_u64 v[26:27], v[40:41], 0, v[26:27]
	v_lshl_add_u64 v[28:29], v[40:41], 0, v[28:29]
	v_or_b32_e32 v73, 52, v33
	global_load_dword v26, v[26:27], off
	v_or_b32_e32 v74, 54, v33
	global_load_dword v25, v[28:29], off
	v_mul_u32_u24_e32 v27, v38, v73
	v_lshlrev_b32_e32 v28, 2, v27
	v_mul_u32_u24_e32 v27, v38, v74
	v_mov_b32_e32 v29, v35
	v_lshlrev_b32_e32 v30, 2, v27
	v_mov_b32_e32 v31, v35
	v_lshl_add_u64 v[28:29], v[40:41], 0, v[28:29]
; #define LAS __attribute__((address_space(3)))
;     ...
;     if (it < I_E) { const PrepItem p = prep_decode(a, l, it);
; #pragma unroll
;         for (int i = 0; i < 32; ++i) tv[i] = __builtin_nontemporal_load(p.src + (size_t)(2 * i + (lane >> 5)) * p.ldw + (lane & 31)); }
;     for (; it < I_E; it += ngw) {
;         const PrepItem p = prep_decode(a, l, it);
; #pragma unroll
;         for (int i = 0; i < 32; ++i) scr[(2 * i + (lane >> 5)) * 33 + (lane & 31)] = tv[i];
;         if (it + ngw < I_E) { const PrepItem q = prep_decode(a, l, it + ngw);
; #pragma unroll
;             for (int i = 0; i < 32; ++i) tv[i] = __builtin_nontemporal_load(q.src + (size_t)(2 * i + (lane >> 5)) * q.ldw + (lane & 31)); }
;         asm volatile("s_waitcnt lgkmcnt(0)" ::: "memory");
;         const int c = lane & 7;
; #pragma unroll
;         for (int j = 0; j < 4; ++j) { const int n = (lane >> 3) + 8 * j; const LAS float* sp = scr + (8 * c) * 33 + n;
	v_lshl_add_u64 v[30:31], v[40:41], 0, v[30:31]
	v_or_b32_e32 v75, 56, v33
	global_load_dword v28, v[28:29], off
	v_or_b32_e32 v76, 58, v33
	global_load_dword v27, v[30:31], off
	v_mul_u32_u24_e32 v29, v38, v75
	v_lshlrev_b32_e32 v30, 2, v29
	v_mul_u32_u24_e32 v29, v38, v76
	v_mov_b32_e32 v31, v35
	v_lshlrev_b32_e32 v44, 2, v29
	v_mov_b32_e32 v45, v35
	v_lshl_add_u64 v[30:31], v[40:41], 0, v[30:31]
	v_lshl_add_u64 v[44:45], v[40:41], 0, v[44:45]
	v_or_b32_e32 v77, 60, v33
	global_load_dword v30, v[30:31], off
	v_or_b32_e32 v78, 62, v33
	global_load_dword v29, v[44:45], off
	v_mul_u32_u24_e32 v31, v38, v77
	v_lshlrev_b32_e32 v44, 2, v31
	v_mul_u32_u24_e32 v31, v38, v78
	v_mov_b32_e32 v45, v35
	v_lshlrev_b32_e32 v38, 2, v31
	v_mov_b32_e32 v39, v35
	v_lshl_add_u64 v[44:45], v[40:41], 0, v[44:45]
	v_lshl_add_u64 v[38:39], v[40:41], 0, v[38:39]
	global_load_dword v32, v[44:45], off
	global_load_dword v31, v[38:39], off
	v_lshlrev_b32_e32 v38, 3, v42
	v_bfe_u32 v79, v42, 3, 3
	v_and_b32_e32 v38, 56, v38
	v_readlane_b32 s5, v252, 37
	v_mul_u32_u24_e32 v39, 0x84, v38
	v_lshlrev_b32_e32 v40, 2, v79
	s_add_i32 s4, s5, 0xffffd780
	v_add_u32_e32 v34, v43, v34
	v_add3_u32 v80, v43, v39, v40
	v_mul_u32_u24_e32 v39, 0x84, v33
	v_add_u32_e32 v40, s5, v37
	v_add_lshl_u32 v89, s4, v37, 11
	s_add_i32 s4, s5, 0xfffff780
	v_or_b32_e32 v81, 8, v79
	v_or_b32_e32 v82, 16, v79
	v_or_b32_e32 v83, 24, v79
	v_lshlrev_b32_e32 v84, 5, v37
	s_lshl_b32 s2, s5, 5
	v_lshlrev_b32_e32 v85, 1, v37
	s_lshl_b32 s18, s5, 1
	v_lshlrev_b32_e32 v86, 15, v37
	s_lshl_b32 s19, s5, 15
	v_lshlrev_b32_e32 v87, 16, v37
	s_lshl_b32 s20, s5, 16
	v_lshlrev_b32_e32 v88, 3, v40
	s_lshl_b32 s21, s5, 3
	s_lshl_b32 s22, s5, 11
	v_add_lshl_u32 v90, s4, v37, 10
	s_lshl_b32 s23, s5, 10
	v_lshlrev_b32_e32 v91, 4, v40
	s_lshl_b32 s24, s5, 4
	s_mov_b64 s[8:9], 0
	v_add_u32_e32 v92, v34, v39
	v_lshlrev_b32_e32 v34, 2, v36
	v_lshlrev_b32_e32 v36, 1, v38
	s_branch .LBB0_320
;     ...
;     for (; it < I_E; it += ngw) {
;         const PrepItem p = prep_decode(a, l, it);
; #pragma unroll
;         for (int i = 0; i < 32; ++i) scr[(2 * i + (lane >> 5)) * 33 + (lane & 31)] = tv[i];
;         if (it + ngw < I_E) { const PrepItem q = prep_decode(a, l, it + ngw);
; #pragma unroll
;             for (int i = 0; i < 32; ++i) tv[i] = __builtin_nontemporal_load(q.src + (size_t)(2 * i + (lane >> 5)) * q.ldw + (lane & 31)); }
.LBB0_318:
	s_or_b64 exec, exec, s[12:13]
	v_mul_u32_u24_e32 v1, v44, v33
	v_lshl_add_u64 v[46:47], v[2:3], 0, v[34:35]
	v_lshlrev_b32_e32 v2, 2, v1
	v_mul_u32_u24_e32 v1, v44, v48
	v_mov_b32_e32 v3, v35
	v_lshlrev_b32_e32 v4, 2, v1
	v_mov_b32_e32 v5, v35
	v_lshl_add_u64 v[2:3], v[46:47], 0, v[2:3]
	v_lshl_add_u64 v[4:5], v[46:47], 0, v[4:5]
	global_load_dword v2, v[2:3], off
	v_mov_b32_e32 v7, v35
	global_load_dword v1, v[4:5], off
	v_mul_u32_u24_e32 v3, v44, v49
	v_lshlrev_b32_e32 v4, 2, v3
	v_mul_u32_u24_e32 v3, v44, v50
	v_mov_b32_e32 v5, v35
	v_lshlrev_b32_e32 v6, 2, v3
	v_lshl_add_u64 v[4:5], v[46:47], 0, v[4:5]
	v_lshl_add_u64 v[6:7], v[46:47], 0, v[6:7]
	global_load_dword v4, v[4:5], off
	v_mov_b32_e32 v9, v35
	global_load_dword v3, v[6:7], off
	v_mul_u32_u24_e32 v5, v44, v51
	v_lshlrev_b32_e32 v6, 2, v5
	v_mul_u32_u24_e32 v5, v44, v52
	v_mov_b32_e32 v7, v35
	v_lshlrev_b32_e32 v8, 2, v5
	v_lshl_add_u64 v[6:7], v[46:47], 0, v[6:7]
	v_lshl_add_u64 v[8:9], v[46:47], 0, v[8:9]
	global_load_dword v6, v[6:7], off
	v_mov_b32_e32 v11, v35
	global_load_dword v5, v[8:9], off
	v_mul_u32_u24_e32 v7, v44, v53
	v_lshlrev_b32_e32 v8, 2, v7
	v_mul_u32_u24_e32 v7, v44, v54
	v_mov_b32_e32 v9, v35
	v_lshlrev_b32_e32 v10, 2, v7
	v_lshl_add_u64 v[8:9], v[46:47], 0, v[8:9]
	v_lshl_add_u64 v[10:11], v[46:47], 0, v[10:11]
	global_load_dword v8, v[8:9], off
	v_mov_b32_e32 v13, v35
	global_load_dword v7, v[10:11], off
	v_mul_u32_u24_e32 v9, v44, v55
	v_lshlrev_b32_e32 v10, 2, v9
	v_mul_u32_u24_e32 v9, v44, v56
	v_mov_b32_e32 v11, v35
	v_lshlrev_b32_e32 v12, 2, v9
	v_lshl_add_u64 v[10:11], v[46:47], 0, v[10:11]
	v_lshl_add_u64 v[12:13], v[46:47], 0, v[12:13]
	global_load_dword v10, v[10:11], off
	v_mov_b32_e32 v15, v35
	global_load_dword v9, v[12:13], off
	v_mul_u32_u24_e32 v11, v44, v57
	v_lshlrev_b32_e32 v12, 2, v11
	v_mul_u32_u24_e32 v11, v44, v58
	v_mov_b32_e32 v13, v35
	v_lshlrev_b32_e32 v14, 2, v11
	v_lshl_add_u64 v[12:13], v[46:47], 0, v[12:13]
	v_lshl_add_u64 v[14:15], v[46:47], 0, v[14:15]
	global_load_dword v12, v[12:13], off
	v_mov_b32_e32 v17, v35
	global_load_dword v11, v[14:15], off
	v_mul_u32_u24_e32 v13, v44, v59
	v_lshlrev_b32_e32 v14, 2, v13
	v_mul_u32_u24_e32 v13, v44, v60
	v_mov_b32_e32 v15, v35
	v_lshlrev_b32_e32 v16, 2, v13
	v_lshl_add_u64 v[14:15], v[46:47], 0, v[14:15]
	v_lshl_add_u64 v[16:17], v[46:47], 0, v[16:17]
	global_load_dword v14, v[14:15], off
	v_mov_b32_e32 v19, v35
	global_load_dword v13, v[16:17], off
	v_mul_u32_u24_e32 v15, v44, v61
	v_lshlrev_b32_e32 v16, 2, v15
	v_mul_u32_u24_e32 v15, v44, v62
	v_mov_b32_e32 v17, v35
	v_lshlrev_b32_e32 v18, 2, v15
	v_lshl_add_u64 v[16:17], v[46:47], 0, v[16:17]
	v_lshl_add_u64 v[18:19], v[46:47], 0, v[18:19]
	global_load_dword v16, v[16:17], off
	v_mov_b32_e32 v21, v35
	global_load_dword v15, v[18:19], off
	v_mul_u32_u24_e32 v17, v44, v63
	v_lshlrev_b32_e32 v18, 2, v17
	v_mul_u32_u24_e32 v17, v44, v64
	v_mov_b32_e32 v19, v35
	v_lshlrev_b32_e32 v20, 2, v17
	v_lshl_add_u64 v[18:19], v[46:47], 0, v[18:19]
	v_lshl_add_u64 v[20:21], v[46:47], 0, v[20:21]
	global_load_dword v18, v[18:19], off
	v_mov_b32_e32 v23, v35
	global_load_dword v17, v[20:21], off
	v_mul_u32_u24_e32 v19, v44, v65
	v_lshlrev_b32_e32 v20, 2, v19
	v_mul_u32_u24_e32 v19, v44, v66
	v_mov_b32_e32 v21, v35
	v_lshlrev_b32_e32 v22, 2, v19
	v_lshl_add_u64 v[20:21], v[46:47], 0, v[20:21]
	v_lshl_add_u64 v[22:23], v[46:47], 0, v[22:23]
	global_load_dword v20, v[20:21], off
	v_mov_b32_e32 v25, v35
	global_load_dword v19, v[22:23], off
	v_mul_u32_u24_e32 v21, v44, v67
	v_lshlrev_b32_e32 v22, 2, v21
	v_mul_u32_u24_e32 v21, v44, v68
	v_mov_b32_e32 v23, v35
	v_lshlrev_b32_e32 v24, 2, v21
	v_lshl_add_u64 v[22:23], v[46:47], 0, v[22:23]
	v_lshl_add_u64 v[24:25], v[46:47], 0, v[24:25]
	global_load_dword v22, v[22:23], off
	v_mov_b32_e32 v27, v35
	global_load_dword v21, v[24:25], off
	v_mul_u32_u24_e32 v23, v44, v69
	v_lshlrev_b32_e32 v24, 2, v23
	v_mul_u32_u24_e32 v23, v44, v70
	v_mov_b32_e32 v25, v35
	v_lshlrev_b32_e32 v26, 2, v23
	v_lshl_add_u64 v[24:25], v[46:47], 0, v[24:25]
	v_lshl_add_u64 v[26:27], v[46:47], 0, v[26:27]
	global_load_dword v24, v[24:25], off
	v_mov_b32_e32 v29, v35
	global_load_dword v23, v[26:27], off
	v_mul_u32_u24_e32 v25, v44, v71
	v_lshlrev_b32_e32 v26, 2, v25
	v_mul_u32_u24_e32 v25, v44, v72
	v_mov_b32_e32 v27, v35
	v_lshlrev_b32_e32 v28, 2, v25
	v_lshl_add_u64 v[26:27], v[46:47], 0, v[26:27]
	v_lshl_add_u64 v[28:29], v[46:47], 0, v[28:29]
	global_load_dword v26, v[26:27], off
	v_mov_b32_e32 v31, v35
	global_load_dword v25, v[28:29], off
	v_mul_u32_u24_e32 v27, v44, v73
	v_lshlrev_b32_e32 v28, 2, v27
	v_mul_u32_u24_e32 v27, v44, v74
	v_mov_b32_e32 v29, v35
	v_lshlrev_b32_e32 v30, 2, v27
	v_lshl_add_u64 v[28:29], v[46:47], 0, v[28:29]
	v_lshl_add_u64 v[30:31], v[46:47], 0, v[30:31]
	global_load_dword v28, v[28:29], off
	v_mov_b32_e32 v95, v35
	global_load_dword v27, v[30:31], off
	v_mul_u32_u24_e32 v29, v44, v75
	v_lshlrev_b32_e32 v30, 2, v29
	v_mul_u32_u24_e32 v29, v44, v76
	v_mov_b32_e32 v31, v35
	v_lshlrev_b32_e32 v94, 2, v29
	v_lshl_add_u64 v[30:31], v[46:47], 0, v[30:31]
	v_lshl_add_u64 v[94:95], v[46:47], 0, v[94:95]
	global_load_dword v30, v[30:31], off
	v_mov_b32_e32 v45, v35
	global_load_dword v29, v[94:95], off
	v_mul_u32_u24_e32 v31, v44, v77
	v_lshlrev_b32_e32 v94, 2, v31
	v_mul_u32_u24_e32 v31, v44, v78
	v_mov_b32_e32 v95, v35
	v_lshlrev_b32_e32 v44, 2, v31
	v_lshl_add_u64 v[94:95], v[46:47], 0, v[94:95]
	v_lshl_add_u64 v[44:45], v[46:47], 0, v[44:45]
	global_load_dword v32, v[94:95], off
	global_load_dword v31, v[44:45], off

; __device__ __forceinline__ void mg_merge(const Args& a) {
;     ...
;     for (size_t i0 = (size_t)blockIdx.x * NTHR + tid; i0 < total; i0 += 4 * step) {
;         u32x4 a0[4], a1[4], a2[4]; float l0[4], l1[4], l2[4];
; #pragma unroll
;         for (int q = 0; q < 4; ++q) { const size_t i = i0 + q * step; if (i < total) { const size_t ht = i >> 3; const int c = (int)(i & 7);
;             l0[q] = dill[(size_t)0 * 6 * NTOK + ht]; l1[q] = dill[(size_t)1 * 6 * NTOK + ht]; l2[q] = dill[(size_t)2 * 6 * NTOK + ht];
;             a0[q] = __builtin_nontemporal_load((const u32x4*)(dilo + ((size_t)0 * 6 * NTOK + ht) * 64 + c * 8));
;             a1[q] = __builtin_nontemporal_load((const u32x4*)(dilo + ((size_t)1 * 6 * NTOK + ht) * 64 + c * 8));
;             a2[q] = __builtin_nontemporal_load((const u32x4*)(dilo + ((size_t)2 * 6 * NTOK + ht) * 64 + c * 8)); } }
.LBB0_648:
	v_lshrrev_b64 v[40:41], 3, v[56:57]
	v_lshl_add_u64 v[42:43], v[40:41], 2, s[82:83]
	s_mov_b32 s2, 0xc0000
	v_add_co_u32_e32 v46, vcc, s2, v42
	v_and_b32_e32 v34, 56, v52
	v_readlane_b32 s4, v252, 8
	v_alignbit_b32 v48, v57, v56, 3
	v_addc_co_u32_e32 v47, vcc, 0, v43, vcc
	s_mov_b32 s2, 0x180000
	v_lshlrev_b32_e32 v34, 1, v34
	v_readlane_b32 s6, v252, 10
	v_readlane_b32 s7, v252, 11
	v_add_u32_e32 v44, 0x30000, v48
	v_mov_b32_e32 v45, v35
	v_add_u32_e32 v48, 0x60000, v48
	v_mov_b32_e32 v49, v35
	v_add_co_u32_e32 v50, vcc, s2, v42
	v_lshl_add_u64 v[58:59], s[6:7], 0, v[34:35]
	s_nop 0
	v_addc_co_u32_e32 v51, vcc, 0, v43, vcc
	global_load_dword v72, v[42:43], off
	global_load_dword v70, v[46:47], off
	global_load_dword v71, v[50:51], off
	v_lshlrev_b64 v[40:41], 7, v[40:41]
	v_lshlrev_b64 v[42:43], 7, v[44:45]
	v_lshlrev_b64 v[48:49], 7, v[48:49]
	v_lshl_add_u64 v[40:41], v[58:59], 0, v[40:41]
	v_lshl_add_u64 v[42:43], v[58:59], 0, v[42:43]
	v_lshl_add_u64 v[48:49], v[58:59], 0, v[48:49]
	global_load_dwordx4 v[44:47], v[40:41], off
	s_nop 0
	global_load_dwordx4 v[40:43], v[42:43], off
	v_readlane_b32 s5, v252, 9
	global_load_dwordx4 v[48:51], v[48:49], off
	v_lshl_add_u64 v[54:55], v[56:57], 0, s[70:71]
	s_mov_b64 s[4:5], 0x180000
	v_cmp_gt_u64_e64 s[4:5], s[4:5], v[54:55]
	s_and_saveexec_b64 s[6:7], s[4:5]
	s_cbranch_execz .LBB0_650
	v_lshrrev_b64 v[2:3], 3, v[54:55]
	v_lshl_add_u64 v[4:5], v[2:3], 2, s[82:83]
	v_add_co_u32_e32 v14, vcc, 0xc0000, v4
	v_lshlrev_b64 v[2:3], 7, v[2:3]
	s_nop 0
	v_addc_co_u32_e32 v15, vcc, 0, v5, vcc
	v_add_co_u32_e32 v16, vcc, 0x180000, v4
	s_nop 1
	v_addc_co_u32_e32 v17, vcc, 0, v5, vcc
	global_load_dword v63, v[4:5], off
	global_load_dword v66, v[14:15], off
	global_load_dword v69, v[16:17], off
	v_lshl_add_u64 v[14:15], v[58:59], 0, v[2:3]
	v_add_co_u32_e32 v16, vcc, 0x1800000, v14
	s_nop 1
	v_addc_co_u32_e32 v17, vcc, 0, v15, vcc
	global_load_dwordx4 v[2:5], v[14:15], off
	global_load_dwordx4 v[26:29], v[16:17], off
	v_add_co_u32_e32 v14, vcc, 0x3000000, v14
	s_nop 1
	v_addc_co_u32_e32 v15, vcc, 0, v15, vcc
	global_load_dwordx4 v[14:17], v[14:15], off
.LBB0_650:
	s_or_b64 exec, exec, s[6:7]
	v_lshl_add_u64 v[60:61], s[52:53], 0, v[56:57]
	s_mov_b64 s[6:7], 0x180000
	v_cmp_gt_u64_e64 s[6:7], s[6:7], v[60:61]
	s_and_saveexec_b64 s[8:9], s[6:7]
	s_cbranch_execz .LBB0_652
	v_lshrrev_b64 v[10:11], 3, v[60:61]
	v_lshl_add_u64 v[12:13], v[10:11], 2, s[82:83]
	v_add_co_u32_e32 v18, vcc, 0xc0000, v12
	v_lshlrev_b64 v[10:11], 7, v[10:11]
	s_nop 0
	v_addc_co_u32_e32 v19, vcc, 0, v13, vcc
	v_add_co_u32_e32 v20, vcc, 0x180000, v12
	v_lshl_add_u64 v[10:11], v[58:59], 0, v[10:11]
	s_nop 0
	v_addc_co_u32_e32 v21, vcc, 0, v13, vcc
	global_load_dword v62, v[12:13], off
	global_load_dword v65, v[18:19], off
	global_load_dword v68, v[20:21], off
	v_add_co_u32_e32 v12, vcc, 0x1800000, v10
	s_nop 1
	v_addc_co_u32_e32 v13, vcc, 0, v11, vcc
	global_load_dwordx4 v[18:21], v[10:11], off
	global_load_dwordx4 v[30:33], v[12:13], off
	v_add_co_u32_e32 v10, vcc, 0x3000000, v10
	s_nop 1
	v_addc_co_u32_e32 v11, vcc, 0, v11, vcc
	global_load_dwordx4 v[10:13], v[10:11], off
.LBB0_652:
	s_or_b64 exec, exec, s[8:9]
	v_lshl_add_u64 v[56:57], s[84:85], 0, v[56:57]
	s_mov_b64 s[8:9], 0x180000
	v_cmp_gt_u64_e64 s[8:9], s[8:9], v[56:57]
	s_and_saveexec_b64 s[14:15], s[8:9]
	s_cbranch_execz .LBB0_654
	v_lshrrev_b64 v[6:7], 3, v[56:57]
	v_lshl_add_u64 v[8:9], v[6:7], 2, s[82:83]
	v_add_co_u32_e32 v22, vcc, 0xc0000, v8
	v_lshlrev_b64 v[6:7], 7, v[6:7]
	s_nop 0
	v_addc_co_u32_e32 v23, vcc, 0, v9, vcc
	v_add_co_u32_e32 v24, vcc, 0x180000, v8
	v_lshl_add_u64 v[6:7], v[58:59], 0, v[6:7]
	s_nop 0
	v_addc_co_u32_e32 v25, vcc, 0, v9, vcc
	global_load_dword v1, v[8:9], off
	global_load_dword v64, v[22:23], off
	global_load_dword v67, v[24:25], off
	v_add_co_u32_e32 v8, vcc, 0x1800000, v6
	s_nop 1
	v_addc_co_u32_e32 v9, vcc, 0, v7, vcc
	global_load_dwordx4 v[22:25], v[6:7], off
	global_load_dwordx4 v[36:39], v[8:9], off
	v_add_co_u32_e32 v6, vcc, 0x3000000, v6
	s_nop 1
	v_addc_co_u32_e32 v7, vcc, 0, v7, vcc
	global_load_dwordx4 v[6:9], v[6:7], off

; __device__ __forceinline__ void fin_combine(const Args& a, int layer, float* outp = nullptr) {
;     ...
;     for (size_t i0 = (size_t)blockIdx.x * NTHR + tid; i0 < n8; i0 += 4 * step) {
;         u32x4 xv[4], y0[4], y1[4];
; #pragma unroll
;         for (int k = 0; k < 4; ++k) { const size_t i = i0 + k * step; if (i < n8) { const size_t e0 = i * 8;
;             xv[k] = __builtin_nontemporal_load((const u32x4*)(xb + e0)); y0[k] = __builtin_nontemporal_load((const u32x4*)(yb + e0)); y1[k] = __builtin_nontemporal_load((const u32x4*)(yb + (size_t)NTOK * D + e0)); } }
.LBB0_1367:
	v_lshl_add_u64 v[44:45], s[22:23], 0, v[60:61]
	v_add_co_u32_e32 v46, vcc, s26, v44
	s_nop 1
	v_addc_co_u32_e32 v47, vcc, 0, v45, vcc
	v_add_co_u32_e32 v68, vcc, 0xbc00000, v44
	s_nop 1
	v_addc_co_u32_e32 v69, vcc, 0, v45, vcc
	v_add_co_u32_e32 v44, vcc, 0xfc00000, v44
	global_load_dwordx4 v[40:43], v[46:47], off
	global_load_dwordx4 v[36:39], v[68:69], off
	v_addc_co_u32_e32 v45, vcc, 0, v45, vcc
	global_load_dwordx4 v[44:47], v[44:45], off
	v_lshl_add_u64 v[68:69], v[70:71], 0, s[70:71]
	v_cmp_gt_u64_e64 s[4:5], s[6:7], v[68:69]
	s_and_saveexec_b64 s[0:1], s[4:5]
	s_cbranch_execz .LBB0_1369
	v_lshl_add_u64 v[20:21], s[22:23], 0, v[64:65]
	v_add_co_u32_e32 v22, vcc, 0x18c00000, v20
	s_nop 1
	v_addc_co_u32_e32 v23, vcc, 0, v21, vcc
	v_add_co_u32_e32 v72, vcc, 0xbc00000, v20
	s_nop 1
	v_addc_co_u32_e32 v73, vcc, 0, v21, vcc
	v_add_co_u32_e32 v20, vcc, 0xfc00000, v20
	global_load_dwordx4 v[0:3], v[22:23], off
	global_load_dwordx4 v[24:27], v[72:73], off
	v_addc_co_u32_e32 v21, vcc, 0, v21, vcc
	global_load_dwordx4 v[20:23], v[20:21], off
.LBB0_1369:
	s_or_b64 exec, exec, s[0:1]
	v_lshl_add_u64 v[74:75], s[52:53], 0, v[70:71]
	v_cmp_gt_u64_e64 s[2:3], s[6:7], v[74:75]
	s_and_saveexec_b64 s[0:1], s[2:3]
	s_cbranch_execz .LBB0_1371
	v_lshl_add_u64 v[16:17], s[22:23], 0, v[48:49]
	v_add_co_u32_e32 v18, vcc, 0x18c00000, v16
	s_nop 1
	v_addc_co_u32_e32 v19, vcc, 0, v17, vcc
	v_add_co_u32_e32 v72, vcc, 0xbc00000, v16
	s_nop 1
	v_addc_co_u32_e32 v73, vcc, 0, v17, vcc
	v_add_co_u32_e32 v16, vcc, 0xfc00000, v16
	global_load_dwordx4 v[4:7], v[18:19], off
	global_load_dwordx4 v[28:31], v[72:73], off
	v_addc_co_u32_e32 v17, vcc, 0, v17, vcc
	global_load_dwordx4 v[16:19], v[16:17], off
.LBB0_1371:
	s_or_b64 exec, exec, s[0:1]
	v_lshl_add_u64 v[72:73], s[84:85], 0, v[70:71]
	v_cmp_gt_u64_e64 s[0:1], s[6:7], v[72:73]
	s_and_saveexec_b64 s[24:25], s[0:1]
	s_cbranch_execz .LBB0_1373
	v_lshl_add_u64 v[8:9], s[22:23], 0, v[54:55]
	v_add_co_u32_e32 v10, vcc, 0x18c00000, v8
	s_nop 1
	v_addc_co_u32_e32 v11, vcc, 0, v9, vcc
	v_add_co_u32_e32 v76, vcc, 0xbc00000, v8
	s_nop 1
	v_addc_co_u32_e32 v77, vcc, 0, v9, vcc
	v_add_co_u32_e32 v8, vcc, 0xfc00000, v8
	global_load_dwordx4 v[12:15], v[10:11], off
	global_load_dwordx4 v[32:35], v[76:77], off
	v_addc_co_u32_e32 v9, vcc, 0, v9, vcc
	global_load_dwordx4 v[8:11], v[8:9], off
